# GQA loop unrolled over the 3-buffer LDS ring: ring bases become immediate offsets, tile loads use saddr addressing, no per-tile VALU address math
# baseline (speedup 1.0000x reference)
; __device__ __forceinline__ int v_st(int k, int c) { const int kk = k;     return ((kk >> 3) * 2 + (c >> 5)) * 512 + ((kk & 7) * 32 + (c & 31)) * 2; }
; __device__ __forceinline__ int v_rd_base(int lane) { return ((lane & 3) << 3) | (((lane >> 2) & 3) << 6) | (((lane >> 4) & 1) << 5) | (((lane >> 5) & 1) << 8); }
; #define SLOAD(i, j) do { const int _row = KROW(j); skn[i] = *(const bf16x8*)(Knp + (size_t)(_row + sr) * ldk + c8 * 8); sv[i] = *(const bf16x8*)(Vp + (size_t)(_row + sr) * ldv + c8 * 8); \
;         if (krw) skr[i] = *(const bf16x8*)(Krp + (size_t)(_row + sr2) * 32 + c4 * 8); } while (0)
; #define SWRITE(b, i) do { *(LAS bf16x8*)(lds + (b) * BUF + kn_st) = skn[i]; *(LAS bf16x8*)(lds + (b) * BUF + v_stw) = sv[i]; if (krw) *(LAS bf16x8*)(lds + (b) * BUF + kr_st) = skr[i]; } while (0)
; #define SWRITEO(boff, i) do { *(LAS bf16x8*)(lds + (boff) + kn_st) = skn[i]; *(LAS bf16x8*)(lds + (boff) + v_stw) = sv[i]; if (krw) *(LAS bf16x8*)(lds + (boff) + kr_st) = skr[i]; } while (0)
; #define SWAIT() asm volatile("s_waitcnt vmcnt(2)" ::: "memory")
; template <int DQK, bool FIXM> ...
;     ...
;     const int sr = tid >> 3, c8 = tid & 7, sr2 = (tid >> 2) & 63, c4 = tid & 3;
;     const bool krw = (DQK == 96) && (tid < 256);
;     const int kn_st = B_KN + swz64(sr, c8), v_stw = B_V + v_st(sr, c8 * 8), kr_st = B_KR + swz32(sr2, c4);
;     const unsigned vb0 = (unsigned)(uintptr_t)lds + B_V + v_rd_base(lane);
;     bf16x8 skn[2], sv[2], skr[2];
;     ...
;     f32x16 pA0, pA1, pB0, pB1; float alA, alB; bf16x8 pa0, pa1, pa2, pa3;
;     int bV = 0, bK = BUF, bW = 2 * BUF;
;     ...
;     __syncthreads();
;     SLOAD(0, 0); asm volatile("s_waitcnt vmcnt(0)" ::: "memory"); SWRITE(0, 0);
;     SLOAD(1, 1); if (2 < NT) SLOAD(0, 2);
;     __syncthreads();
;     qkt<DQK>(pA0, pA1, lds, qr, r32, hi, negm);
;     if (FIXM) { alA = 1.f; _Pragma("unroll") for (int r = 0; r < 16; ++r) pA0[r] = __builtin_amdgcn_exp2f(pA0[r]); } else partialSM<true>(pA0, pA1, m_reg, negm, alA);
;     SWAIT(); SWRITEO(BUF, 1);
.LBB0_496:
	s_lshr_b32 s8, s8, 6
	s_and_b64 s[0:1], s[10:11], exec
	s_cselect_b32 s8, s8, s14
	s_and_b32 s9, s8, 7
	s_lshl_b64 s[0:1], s[4:5], 10
	s_add_u32 s0, s15, s0
	s_addc_u32 s1, s16, s1
	s_lshl_b32 s34, s9, 6
	s_lshl_b32 s9, s9, 7
	s_add_u32 s38, s0, s9
	s_addc_u32 s39, s1, 0
	s_lshl_b32 s0, s8, 5
	s_and_b32 s8, s0, 0x80
	s_add_u32 s0, s19, s8
	v_add_u32_e32 v16, s36, v1
	s_addc_u32 s1, s20, 0
	v_ashrrev_i32_e32 v17, 31, v16
	s_add_u32 s8, s23, s8
	v_lshl_add_u64 v[4:5], s[38:39], 0, v[192:193]
	v_lshlrev_b32_e32 v2, 1, v200
	v_lshlrev_b64 v[16:17], 8, v[16:17]
	s_addc_u32 s9, s24, 0
	v_lshl_add_u64 v[4:5], v[4:5], 0, v[2:3]
	v_lshl_add_u64 v[34:35], s[0:1], 0, v[16:17]
	v_lshlrev_b32_e32 v2, 1, v188
	v_lshl_add_u64 v[34:35], v[34:35], 0, v[2:3]
	v_lshl_add_u64 v[16:17], s[8:9], 0, v[16:17]
	global_load_dwordx4 v[114:117], v[4:5], off
	global_load_dwordx4 v[12:15], v[4:5], off offset:32
	global_load_dwordx4 v[8:11], v[4:5], off offset:64
	s_nop 0
	global_load_dwordx4 v[4:7], v[4:5], off offset:96
	s_barrier
	v_lshl_add_u64 v[16:17], v[16:17], 0, v[2:3]
	global_load_dwordx4 v[34:37], v[34:35], off
	s_nop 0
	global_load_dwordx4 v[38:41], v[16:17], off
	s_lshl_b32 s36, s31, 6
	s_sub_i32 s36, s29, s36
	s_and_b64 s[10:11], s[10:11], exec
	s_cselect_b32 s10, s12, s36
	v_add_u32_e32 v16, s10, v191
	v_ashrrev_i32_e32 v17, 31, v16
	v_lshlrev_b64 v[16:17], 8, v[16:17]
	v_add_u32_e32 v42, s10, v189
	v_lshl_add_u64 v[44:45], s[0:1], 0, v[16:17]
	v_lshl_add_u64 v[16:17], s[8:9], 0, v[16:17]
	s_waitcnt vmcnt(0)
	v_lshl_add_u64 v[44:45], v[44:45], 0, v[2:3]
	v_lshl_add_u64 v[16:17], v[16:17], 0, v[2:3]
	v_ashrrev_i32_e32 v43, 31, v42
	global_load_dwordx4 v[58:61], v[44:45], off
	global_load_dwordx4 v[62:65], v[16:17], off
	v_lshlrev_b64 v[16:17], 8, v[42:43]
	v_lshl_add_u64 v[42:43], s[0:1], 0, v[16:17]
	v_lshl_add_u64 v[16:17], s[8:9], 0, v[16:17]
	v_lshl_add_u64 v[42:43], v[42:43], 0, v[2:3]
	v_lshl_add_u64 v[16:17], v[16:17], 0, v[2:3]
	global_load_dwordx4 v[118:121], v[42:43], off
	global_load_dwordx4 v[122:125], v[16:17], off
	v_add_u32_e32 v106, 0, v187
	v_add_u32_e32 v46, v208, v209
	v_add_u32_e32 v107, 0, v214
	v_add_u32_e32 v16, v208, v210
	v_add_u32_e32 v17, v208, v211
	v_add_u32_e32 v57, v208, v212
	v_mov_b32_e32 v136, 0
	s_mov_b32 s10, 0xa000
	s_movk_i32 s11, 0x5000
	v_mov_b32_e32 v137, v221
	v_mov_b32_e32 v50, 0
	v_mov_b32_e32 v42, v136
	v_mov_b32_e32 v43, v136
	v_mov_b32_e32 v48, v136
	v_mov_b32_e32 v49, v136
	v_mov_b32_e32 v51, v136
	v_mov_b32_e32 v56, v136
	v_lshl_add_u64 v[134:135], s[8:9], 0, v[2:3]
	s_mov_b64 s[44:45], s[8:9]
	s_waitcnt vmcnt(5)
	ds_write_b128 v106, v[34:37]
	s_waitcnt vmcnt(4)
	ds_write_b128 v107, v[38:41] offset:12288
	s_waitcnt lgkmcnt(0)
	s_barrier
	ds_read_b128 v[34:37], v46
	ds_read_b128 v[38:41], v46 offset:4096
	s_waitcnt lgkmcnt(1)
	v_mfma_f32_32x32x16_bf16 v[82:97], v[34:37], v[114:117], v[18:33]
	ds_read_b128 v[34:37], v16
	ds_read_b128 v[44:47], v17
	ds_read_b128 v[52:55], v17 offset:4096
	ds_read_b128 v[98:101], v57
	ds_read_b128 v[102:105], v57 offset:4096
	v_mov_b32_e32 v57, v136
	s_waitcnt lgkmcnt(5)
	v_mfma_f32_32x32x16_bf16 v[66:81], v[38:41], v[114:117], v[18:33]
	ds_read_b128 v[38:41], v16 offset:4096
	s_waitcnt vmcnt(2)
	v_lshl_add_u64 v[16:17], s[0:1], 0, v[2:3]
	s_mov_b64 s[42:43], s[0:1]
	s_add_i32 s0, s30, -1
	s_waitcnt vmcnt(3)
	ds_write_b128 v106, v[58:61] offset:20480
	s_waitcnt vmcnt(2)
	ds_write_b128 v107, v[62:65] offset:32768
	v_mov_b32_e32 v58, v136
	v_mov_b32_e32 v59, v136
	s_waitcnt lgkmcnt(7)
	v_mfma_f32_32x32x16_bf16 v[82:97], v[34:37], v[12:15], v[82:97]
	v_mov_b32_e32 v34, 0
	v_mov_b32_e32 v35, v136
	v_mov_b32_e32 v36, v136
	v_mov_b32_e32 v37, v136
	v_mov_b32_e32 v60, v136
	v_mov_b32_e32 v61, v136
	v_mov_b32_e32 v62, v136
	s_waitcnt lgkmcnt(2)
	v_mfma_f32_32x32x16_bf16 v[66:81], v[38:41], v[12:15], v[66:81]
	v_mov_b32_e32 v38, v136
	v_mov_b32_e32 v39, v136
	v_mov_b32_e32 v40, v136
	v_mov_b32_e32 v41, v136
	v_mov_b32_e32 v63, v136
	v_mov_b32_e32 v64, v136
	v_mov_b32_e32 v65, v136
	v_mfma_f32_32x32x16_bf16 v[82:97], v[44:47], v[8:11], v[82:97]
	v_mov_b32_e32 v44, v136
	v_mov_b32_e32 v45, v136
	v_mov_b32_e32 v46, v136
	v_mov_b32_e32 v47, v136
	v_mfma_f32_32x32x16_bf16 v[66:81], v[52:55], v[8:11], v[66:81]
	v_mov_b32_e32 v52, v136
	v_mov_b32_e32 v53, v136
	v_mov_b32_e32 v54, v136
	v_mov_b32_e32 v55, v136
	v_mfma_f32_32x32x16_bf16 v[82:97], v[98:101], v[4:7], v[82:97]
	v_mfma_f32_32x32x16_bf16 v[66:81], v[102:105], v[4:7], v[66:81]
	s_nop 10
	v_exp_f32_e32 v143, v82
	v_exp_f32_e32 v145, v83
	v_exp_f32_e32 v141, v84
	v_exp_f32_e32 v144, v85
	v_exp_f32_e32 v139, v86
	v_exp_f32_e32 v142, v87
	v_exp_f32_e32 v138, v88
	v_exp_f32_e32 v140, v89
	v_exp_f32_e32 v151, v90
	v_exp_f32_e32 v153, v91
	v_exp_f32_e32 v149, v92
	v_exp_f32_e32 v152, v93
	v_exp_f32_e32 v147, v94
	v_exp_f32_e32 v150, v95
	v_exp_f32_e32 v146, v96
	v_exp_f32_e32 v148, v97
	v_add_u32_e32 v223, v208, v209
	v_add_u32_e32 v252, v208, v210
	v_add_u32_e32 v253, v208, v211
	v_lshlrev_b32_e32 v137, 8, v221
	v_add_u32_e32 v137, v137, v2
	v_add_u32_e32 v2, v208, v212
	s_movk_i32 s50, 0xffc0
; __device__ __forceinline__ void finishSM(f32x16& p0, f32x16& p1, float alpha, float& l_reg, bf16x8& pa0, bf16x8& pa1, bf16x8& pa2, bf16x8& pa3) {
; #pragma unroll
;     for (int r = 0; r < 16; ++r) p1[r] = EXP_PROBE ? fmaf(p1[r], 0.001f, 1.f) : __builtin_amdgcn_exp2f(p1[r]);
;     float ps = 0.f;
; #pragma unroll
;     for (int r = 0; r < 16; ++r) ps += p0[r];
; #pragma unroll
;     for (int r = 0; r < 16; ++r) ps += p1[r];
;     { auto rr = __builtin_amdgcn_permlane32_swap(__float_as_uint(ps), __float_as_uint(ps), false, false);
;       ps = __uint_as_float(rr[0]) + __uint_as_float(rr[1]); }
;     l_reg = l_reg * alpha + ps;
;     ATT_PKN(p0, 0, pa0); ATT_PKN(p0, 8, pa1); ATT_PKN(p1, 0, pa2); ATT_PKN(p1, 8, pa3);
; }
; template <int DQK> __device__ __forceinline__ void qkt(f32x16& p0, f32x16& p1, const LAS char* buf, const bf16x8* qr, int r32, int hi, const f32x16& negm) {
; #pragma unroll
;     for (int d0 = 0; d0 < 4; ++d0) { const int ch = d0 * 2 + hi;
;         const bf16x8 b0 = *(const LAS bf16x8*)(buf + B_KN + swz64(r32, ch));
;         const bf16x8 b1 = *(const LAS bf16x8*)(buf + B_KN + swz64(32 + r32, ch));
;         p0 = __builtin_amdgcn_mfma_f32_32x32x16_bf16(b0, qr[d0], d0 == 0 ? negm : p0, 0, 0, 0);
;         p1 = __builtin_amdgcn_mfma_f32_32x32x16_bf16(b1, qr[d0], d0 == 0 ? negm : p1, 0, 0, 0); }
;     if constexpr (DQK == 96) {
; #pragma unroll
;         for (int d0 = 0; d0 < 2; ++d0) { const int ch = d0 * 2 + hi;
;             const bf16x8 b0 = *(const LAS bf16x8*)(buf + B_KR + swz32(r32, ch));
;             const bf16x8 b1 = *(const LAS bf16x8*)(buf + B_KR + swz32(32 + r32, ch));
;             p0 = __builtin_amdgcn_mfma_f32_32x32x16_bf16(b0, qr[4 + d0], p0, 0, 0, 0);
;             p1 = __builtin_amdgcn_mfma_f32_32x32x16_bf16(b1, qr[4 + d0], p1, 0, 0, 0); }
;     }
; }
; template <int D0> __device__ __forceinline__ void pv_one(f32x16& od, unsigned vb, bf16x8 pa0, bf16x8 pa1, bf16x8 pa2, bf16x8 pa3) {
;     const s16x4 l0 = tr_read<v_rd_off(D0, 0, 0)>(vb), h0 = tr_read<v_rd_off(D0, 0, 1)>(vb), l1 = tr_read<v_rd_off(D0, 1, 0)>(vb), h1 = tr_read<v_rd_off(D0, 1, 1)>(vb);
;     const s16x4 l2 = tr_read<v_rd_off(D0, 2, 0)>(vb), h2 = tr_read<v_rd_off(D0, 2, 1)>(vb), l3 = tr_read<v_rd_off(D0, 3, 0)>(vb), h3 = tr_read<v_rd_off(D0, 3, 1)>(vb);
;     asm volatile("s_waitcnt lgkmcnt(0)" ::: "memory"); SBAR();
.LBB0_497:
	s_waitcnt lgkmcnt(0)
	s_barrier
	ds_read_b128 v[224:227], v223 offset:20480
	ds_read_b128 v[228:231], v223 offset:24576
	ds_read_b128 v[232:235], v252 offset:20480
	ds_read_b128 v[236:239], v252 offset:24576
	ds_read_b128 v[240:243], v253 offset:20480
	ds_read_b128 v[244:247], v253 offset:24576
	ds_read_b128 v[248:251], v2 offset:20480
	v_exp_f32_e32 v66, v66
	v_exp_f32_e32 v67, v67
	v_exp_f32_e32 v68, v68
	v_exp_f32_e32 v69, v69
	v_exp_f32_e32 v70, v70
	v_exp_f32_e32 v71, v71
	v_exp_f32_e32 v72, v72
	v_exp_f32_e32 v73, v73
	s_waitcnt lgkmcnt(6)
	v_mfma_f32_32x32x16_bf16 v[98:113], v[224:227], v[114:117], v[18:33]
	ds_read_b128 v[224:227], v2 offset:24576
	v_exp_f32_e32 v74, v74
	v_exp_f32_e32 v75, v75
	v_exp_f32_e32 v76, v76
	v_cvt_pk_bf16_f32 v156, v143, v145
	v_cvt_pk_bf16_f32 v157, v141, v144
	v_add_f32_e32 v164, 0, v143
	v_add_f32_e32 v164, v145, v164
	v_add_f32_e32 v164, v141, v164
	s_waitcnt lgkmcnt(6)
	v_mfma_f32_32x32x16_bf16 v[82:97], v[228:231], v[114:117], v[18:33]
	v_exp_f32_e32 v77, v77
	v_exp_f32_e32 v78, v78
	v_exp_f32_e32 v79, v79
	v_cvt_pk_bf16_f32 v158, v139, v142
	v_cvt_pk_bf16_f32 v159, v138, v140
	v_add_f32_e32 v164, v144, v164
	v_add_f32_e32 v164, v139, v164
	v_add_f32_e32 v164, v142, v164
	s_waitcnt lgkmcnt(5)
	v_mfma_f32_32x32x16_bf16 v[98:113], v[232:235], v[12:15], v[98:113]
	v_exp_f32_e32 v80, v80
	v_exp_f32_e32 v81, v81
	v_cvt_pk_bf16_f32 v160, v151, v153
	v_cvt_pk_bf16_f32 v161, v149, v152
	v_cvt_pk_bf16_f32 v162, v147, v150
	v_cvt_pk_bf16_f32 v163, v146, v148
	v_add_f32_e32 v164, v138, v164
	v_add_f32_e32 v164, v140, v164
	v_add_f32_e32 v164, v151, v164
	s_waitcnt lgkmcnt(4)
	v_mfma_f32_32x32x16_bf16 v[82:97], v[236:239], v[12:15], v[82:97]
	v_add_f32_e32 v164, v153, v164
	v_add_f32_e32 v164, v149, v164
	v_add_f32_e32 v164, v152, v164
	v_add_f32_e32 v164, v147, v164
	v_add_f32_e32 v164, v150, v164
	v_add_f32_e32 v164, v146, v164
	v_add_f32_e32 v164, v148, v164
	s_waitcnt lgkmcnt(3)
	v_mfma_f32_32x32x16_bf16 v[98:113], v[240:243], v[8:11], v[98:113]
	ds_read_b64_tr_b16 v[138:139], v213 offset:0
	ds_read_b64_tr_b16 v[140:141], v213 offset:1024
	ds_read_b64_tr_b16 v[142:143], v213 offset:2048
	ds_read_b64_tr_b16 v[144:145], v213 offset:3072
	v_add_f32_e32 v164, v66, v164
	v_add_f32_e32 v164, v67, v164
	v_add_f32_e32 v164, v68, v164
	v_add_f32_e32 v164, v69, v164
	s_waitcnt lgkmcnt(6)
	v_mfma_f32_32x32x16_bf16 v[82:97], v[244:247], v[8:11], v[82:97]
	ds_read_b64_tr_b16 v[146:147], v213 offset:4096
	ds_read_b64_tr_b16 v[148:149], v213 offset:5120
	ds_read_b64_tr_b16 v[150:151], v213 offset:6144
	ds_read_b64_tr_b16 v[152:153], v213 offset:7168
	v_add_f32_e32 v164, v70, v164
	v_add_f32_e32 v164, v71, v164
	v_add_f32_e32 v164, v72, v164
	v_add_f32_e32 v164, v73, v164
	s_waitcnt lgkmcnt(9)
	v_mfma_f32_32x32x16_bf16 v[98:113], v[248:251], v[4:7], v[98:113]
	v_add_f32_e32 v164, v74, v164
	v_add_f32_e32 v164, v75, v164
	v_add_f32_e32 v164, v76, v164
	v_add_f32_e32 v164, v77, v164
	s_waitcnt lgkmcnt(8)
	v_mfma_f32_32x32x16_bf16 v[82:97], v[224:227], v[4:7], v[82:97]
	ds_read_b64_tr_b16 v[224:225], v213 offset:512
	ds_read_b64_tr_b16 v[226:227], v213 offset:1536
	ds_read_b64_tr_b16 v[228:229], v213 offset:2560
	ds_read_b64_tr_b16 v[230:231], v213 offset:3584
	ds_read_b64_tr_b16 v[232:233], v213 offset:4608
	ds_read_b64_tr_b16 v[234:235], v213 offset:5632
	ds_read_b64_tr_b16 v[236:237], v213 offset:6656
	ds_read_b64_tr_b16 v[238:239], v213 offset:7680
	s_waitcnt lgkmcnt(8)
	v_mfma_f32_32x32x16_bf16 v[50:65], v[138:141], v[156:159], v[50:65]
	v_add_f32_e32 v164, v78, v164
	v_add_f32_e32 v164, v79, v164
	v_add_f32_e32 v164, v80, v164
	v_add_f32_e32 v154, v81, v164
	v_mov_b32_e32 v155, v154
	v_mfma_f32_32x32x16_bf16 v[50:65], v[142:145], v[160:163], v[50:65]
	v_cvt_pk_bf16_f32 v66, v66, v67
	v_cvt_pk_bf16_f32 v67, v68, v69
	v_cvt_pk_bf16_f32 v68, v70, v71
	v_cvt_pk_bf16_f32 v69, v72, v73
	v_cvt_pk_bf16_f32 v70, v74, v75
	v_cvt_pk_bf16_f32 v71, v76, v77
	v_cvt_pk_bf16_f32 v72, v78, v79
	v_cvt_pk_bf16_f32 v73, v80, v81
	v_permlane32_swap_b32_e32 v154, v155
	v_mfma_f32_32x32x16_bf16 v[50:65], v[146:149], v[66:69], v[50:65]
	s_add_i32 s8, s13, -1
	s_cmp_lt_u32 s8, s31
	s_cselect_b32 s9, 0, s31
	s_cselect_b32 s35, s12, s29
	s_lshl_b32 s9, s9, 6
	s_sub_i32 s9, s35, s9
	s_add_i32 s52, s9, s50
	s_ashr_i32 s53, s52, 31
	s_lshl_b64 s[52:53], s[52:53], 8
	s_add_u32 s54, s42, s52
	v_mfma_f32_32x32x16_bf16 v[50:65], v[150:153], v[70:73], v[50:65]
	s_addc_u32 s55, s43, s53
	s_add_u32 s56, s44, s52
	s_addc_u32 s57, s45, s53
	global_load_dwordx4 v[130:133], v137, s[54:55]
	global_load_dwordx4 v[126:129], v137, s[56:57]
	s_waitcnt lgkmcnt(0)
	v_mfma_f32_32x32x16_bf16 v[34:49], v[224:227], v[156:159], v[34:49]
	s_waitcnt vmcnt(2)
	ds_write_b128 v187, v[118:121] offset:40960
	ds_write_b128 v214, v[122:125] offset:53248
	v_exp_f32_e32 v168, v98
	v_exp_f32_e32 v169, v99
	v_mfma_f32_32x32x16_bf16 v[34:49], v[228:231], v[160:163], v[34:49]
	v_exp_f32_e32 v170, v100
	v_exp_f32_e32 v171, v101
	v_exp_f32_e32 v172, v102
	v_exp_f32_e32 v173, v103
	v_mfma_f32_32x32x16_bf16 v[34:49], v[232:235], v[66:69], v[34:49]
	v_exp_f32_e32 v174, v104
	v_exp_f32_e32 v175, v105
	v_exp_f32_e32 v176, v106
	v_exp_f32_e32 v177, v107
	v_exp_f32_e32 v178, v108
	v_mfma_f32_32x32x16_bf16 v[34:49], v[236:239], v[70:73], v[34:49]
	v_exp_f32_e32 v179, v109
	v_exp_f32_e32 v180, v110
	v_exp_f32_e32 v181, v111
	v_exp_f32_e32 v182, v112
	v_exp_f32_e32 v183, v113
	s_waitcnt lgkmcnt(0)
	s_barrier
; __device__ __forceinline__ void finishSM(f32x16& p0, f32x16& p1, float alpha, float& l_reg, bf16x8& pa0, bf16x8& pa1, bf16x8& pa2, bf16x8& pa3) {
; #pragma unroll
;     for (int r = 0; r < 16; ++r) p1[r] = EXP_PROBE ? fmaf(p1[r], 0.001f, 1.f) : __builtin_amdgcn_exp2f(p1[r]);
;     float ps = 0.f;
; #pragma unroll
;     for (int r = 0; r < 16; ++r) ps += p0[r];
; #pragma unroll
;     for (int r = 0; r < 16; ++r) ps += p1[r];
;     { auto rr = __builtin_amdgcn_permlane32_swap(__float_as_uint(ps), __float_as_uint(ps), false, false);
;       ps = __uint_as_float(rr[0]) + __uint_as_float(rr[1]); }
;     l_reg = l_reg * alpha + ps;
;     ATT_PKN(p0, 0, pa0); ATT_PKN(p0, 8, pa1); ATT_PKN(p1, 0, pa2); ATT_PKN(p1, 8, pa3);
; }
; template <int DQK> __device__ __forceinline__ void qkt(f32x16& p0, f32x16& p1, const LAS char* buf, const bf16x8* qr, int r32, int hi, const f32x16& negm) {
; #pragma unroll
;     for (int d0 = 0; d0 < 4; ++d0) { const int ch = d0 * 2 + hi;
;         const bf16x8 b0 = *(const LAS bf16x8*)(buf + B_KN + swz64(r32, ch));
;         const bf16x8 b1 = *(const LAS bf16x8*)(buf + B_KN + swz64(32 + r32, ch));
;         p0 = __builtin_amdgcn_mfma_f32_32x32x16_bf16(b0, qr[d0], d0 == 0 ? negm : p0, 0, 0, 0);
;         p1 = __builtin_amdgcn_mfma_f32_32x32x16_bf16(b1, qr[d0], d0 == 0 ? negm : p1, 0, 0, 0); }
;     if constexpr (DQK == 96) {
; #pragma unroll
;         for (int d0 = 0; d0 < 2; ++d0) { const int ch = d0 * 2 + hi;
;             const bf16x8 b0 = *(const LAS bf16x8*)(buf + B_KR + swz32(r32, ch));
;             const bf16x8 b1 = *(const LAS bf16x8*)(buf + B_KR + swz32(32 + r32, ch));
;             p0 = __builtin_amdgcn_mfma_f32_32x32x16_bf16(b0, qr[4 + d0], p0, 0, 0, 0);
;             p1 = __builtin_amdgcn_mfma_f32_32x32x16_bf16(b1, qr[4 + d0], p1, 0, 0, 0); }
;     }
; }
; template <int D0> __device__ __forceinline__ void pv_one(f32x16& od, unsigned vb, bf16x8 pa0, bf16x8 pa1, bf16x8 pa2, bf16x8 pa3) {
;     const s16x4 l0 = tr_read<v_rd_off(D0, 0, 0)>(vb), h0 = tr_read<v_rd_off(D0, 0, 1)>(vb), l1 = tr_read<v_rd_off(D0, 1, 0)>(vb), h1 = tr_read<v_rd_off(D0, 1, 1)>(vb);
;     const s16x4 l2 = tr_read<v_rd_off(D0, 2, 0)>(vb), h2 = tr_read<v_rd_off(D0, 2, 1)>(vb), l3 = tr_read<v_rd_off(D0, 3, 0)>(vb), h3 = tr_read<v_rd_off(D0, 3, 1)>(vb);
;     asm volatile("s_waitcnt lgkmcnt(0)" ::: "memory"); SBAR();
	ds_read_b128 v[224:227], v223 offset:40960
	ds_read_b128 v[228:231], v223 offset:45056
	ds_read_b128 v[232:235], v252 offset:40960
	ds_read_b128 v[236:239], v252 offset:45056
	ds_read_b128 v[240:243], v253 offset:40960
	ds_read_b128 v[244:247], v253 offset:45056
	ds_read_b128 v[248:251], v2 offset:40960
	v_exp_f32_e32 v82, v82
	v_exp_f32_e32 v83, v83
	v_exp_f32_e32 v84, v84
	v_exp_f32_e32 v85, v85
	v_exp_f32_e32 v86, v86
	v_exp_f32_e32 v87, v87
	v_exp_f32_e32 v88, v88
	v_exp_f32_e32 v89, v89
	s_waitcnt lgkmcnt(6)
	v_mfma_f32_32x32x16_bf16 v[98:113], v[224:227], v[114:117], v[18:33]
	ds_read_b128 v[224:227], v2 offset:45056
	v_exp_f32_e32 v90, v90
	v_exp_f32_e32 v91, v91
	v_exp_f32_e32 v92, v92
	v_cvt_pk_bf16_f32 v156, v168, v169
	v_cvt_pk_bf16_f32 v157, v170, v171
	v_add_f32_e32 v164, 0, v168
	v_add_f32_e32 v164, v169, v164
	v_add_f32_e32 v164, v170, v164
	s_waitcnt lgkmcnt(6)
	v_mfma_f32_32x32x16_bf16 v[66:81], v[228:231], v[114:117], v[18:33]
	v_exp_f32_e32 v93, v93
	v_exp_f32_e32 v94, v94
	v_exp_f32_e32 v95, v95
	v_cvt_pk_bf16_f32 v158, v172, v173
	v_cvt_pk_bf16_f32 v159, v174, v175
	v_add_f32_e32 v164, v171, v164
	v_add_f32_e32 v164, v172, v164
	v_add_f32_e32 v164, v173, v164
	s_waitcnt lgkmcnt(5)
	v_mfma_f32_32x32x16_bf16 v[98:113], v[232:235], v[12:15], v[98:113]
	v_exp_f32_e32 v96, v96
	v_exp_f32_e32 v97, v97
	v_cvt_pk_bf16_f32 v160, v176, v177
	v_cvt_pk_bf16_f32 v161, v178, v179
	v_cvt_pk_bf16_f32 v162, v180, v181
	v_cvt_pk_bf16_f32 v163, v182, v183
	v_add_f32_e32 v164, v174, v164
	v_add_f32_e32 v164, v175, v164
	v_add_f32_e32 v164, v176, v164
	s_waitcnt lgkmcnt(4)
	v_mfma_f32_32x32x16_bf16 v[66:81], v[236:239], v[12:15], v[66:81]
	v_add_f32_e32 v164, v177, v164
	v_add_f32_e32 v164, v178, v164
	v_add_f32_e32 v164, v179, v164
	v_add_f32_e32 v164, v180, v164
	v_add_f32_e32 v164, v181, v164
	v_add_f32_e32 v164, v182, v164
	v_add_f32_e32 v164, v183, v164
	s_waitcnt lgkmcnt(3)
	v_mfma_f32_32x32x16_bf16 v[98:113], v[240:243], v[8:11], v[98:113]
	ds_read_b64_tr_b16 v[168:169], v213 offset:20480
	ds_read_b64_tr_b16 v[170:171], v213 offset:21504
	ds_read_b64_tr_b16 v[172:173], v213 offset:22528
	ds_read_b64_tr_b16 v[174:175], v213 offset:23552
	v_add_f32_e32 v164, v82, v164
	v_add_f32_e32 v164, v83, v164
	v_add_f32_e32 v164, v84, v164
	v_add_f32_e32 v164, v85, v164
	s_waitcnt lgkmcnt(6)
	v_mfma_f32_32x32x16_bf16 v[66:81], v[244:247], v[8:11], v[66:81]
	ds_read_b64_tr_b16 v[176:177], v213 offset:24576
	ds_read_b64_tr_b16 v[178:179], v213 offset:25600
	ds_read_b64_tr_b16 v[180:181], v213 offset:26624
	ds_read_b64_tr_b16 v[182:183], v213 offset:27648
	v_add_f32_e32 v164, v86, v164
	v_add_f32_e32 v164, v87, v164
	v_add_f32_e32 v164, v88, v164
	v_add_f32_e32 v164, v89, v164
	s_waitcnt lgkmcnt(9)
	v_mfma_f32_32x32x16_bf16 v[98:113], v[248:251], v[4:7], v[98:113]
	v_add_f32_e32 v164, v90, v164
	v_add_f32_e32 v164, v91, v164
	v_add_f32_e32 v164, v92, v164
	v_add_f32_e32 v164, v93, v164
	s_waitcnt lgkmcnt(8)
	v_mfma_f32_32x32x16_bf16 v[66:81], v[224:227], v[4:7], v[66:81]
	ds_read_b64_tr_b16 v[224:225], v213 offset:20992
	ds_read_b64_tr_b16 v[226:227], v213 offset:22016
	ds_read_b64_tr_b16 v[228:229], v213 offset:23040
	ds_read_b64_tr_b16 v[230:231], v213 offset:24064
	ds_read_b64_tr_b16 v[232:233], v213 offset:25088
	ds_read_b64_tr_b16 v[234:235], v213 offset:26112
	ds_read_b64_tr_b16 v[236:237], v213 offset:27136
	ds_read_b64_tr_b16 v[238:239], v213 offset:28160
	s_waitcnt lgkmcnt(8)
	v_mfma_f32_32x32x16_bf16 v[50:65], v[168:171], v[156:159], v[50:65]
	v_add_f32_e32 v164, v94, v164
	v_add_f32_e32 v164, v95, v164
	v_add_f32_e32 v164, v96, v164
	v_add_f32_e32 v164, v97, v164
	v_mov_b32_e32 v165, v164
	v_mfma_f32_32x32x16_bf16 v[50:65], v[172:175], v[160:163], v[50:65]
	v_cvt_pk_bf16_f32 v82, v82, v83
	v_cvt_pk_bf16_f32 v83, v84, v85
	v_cvt_pk_bf16_f32 v84, v86, v87
	v_cvt_pk_bf16_f32 v85, v88, v89
	v_cvt_pk_bf16_f32 v86, v90, v91
	v_cvt_pk_bf16_f32 v87, v92, v93
	v_cvt_pk_bf16_f32 v88, v94, v95
	v_cvt_pk_bf16_f32 v89, v96, v97
	v_permlane32_swap_b32_e32 v164, v165
	v_mfma_f32_32x32x16_bf16 v[50:65], v[176:179], v[82:85], v[50:65]
	v_mfma_f32_32x32x16_bf16 v[50:65], v[180:183], v[86:89], v[50:65]
	s_cmp_ge_u32 s13, s30
	s_cbranch_scc1 .Lgqa_b_noload_0
	s_cmp_lt_u32 s13, s31
	s_cselect_b32 s9, 0, s31
	s_cselect_b32 s35, s12, s29
	s_lshl_b32 s9, s9, 6
	s_sub_i32 s9, s35, s9
	s_add_i32 s52, s9, s50
	s_add_i32 s52, s52, 64
	s_ashr_i32 s53, s52, 31
	s_lshl_b64 s[52:53], s[52:53], 8
	s_add_u32 s54, s42, s52
	s_addc_u32 s55, s43, s53
	s_add_u32 s56, s44, s52
	s_addc_u32 s57, s45, s53
	global_load_dwordx4 v[118:121], v137, s[54:55]
	global_load_dwordx4 v[122:125], v137, s[56:57]
; __device__ __forceinline__ void finishSM(f32x16& p0, f32x16& p1, float alpha, float& l_reg, bf16x8& pa0, bf16x8& pa1, bf16x8& pa2, bf16x8& pa3) {
; #pragma unroll
;     for (int r = 0; r < 16; ++r) p1[r] = EXP_PROBE ? fmaf(p1[r], 0.001f, 1.f) : __builtin_amdgcn_exp2f(p1[r]);
;     float ps = 0.f;
; #pragma unroll
;     for (int r = 0; r < 16; ++r) ps += p0[r];
; #pragma unroll
;     for (int r = 0; r < 16; ++r) ps += p1[r];
;     { auto rr = __builtin_amdgcn_permlane32_swap(__float_as_uint(ps), __float_as_uint(ps), false, false);
;       ps = __uint_as_float(rr[0]) + __uint_as_float(rr[1]); }
;     l_reg = l_reg * alpha + ps;
;     ATT_PKN(p0, 0, pa0); ATT_PKN(p0, 8, pa1); ATT_PKN(p1, 0, pa2); ATT_PKN(p1, 8, pa3);
; }
; template <int DQK> __device__ __forceinline__ void qkt(f32x16& p0, f32x16& p1, const LAS char* buf, const bf16x8* qr, int r32, int hi, const f32x16& negm) {
; #pragma unroll
;     for (int d0 = 0; d0 < 4; ++d0) { const int ch = d0 * 2 + hi;
;         const bf16x8 b0 = *(const LAS bf16x8*)(buf + B_KN + swz64(r32, ch));
;         const bf16x8 b1 = *(const LAS bf16x8*)(buf + B_KN + swz64(32 + r32, ch));
;         p0 = __builtin_amdgcn_mfma_f32_32x32x16_bf16(b0, qr[d0], d0 == 0 ? negm : p0, 0, 0, 0);
;         p1 = __builtin_amdgcn_mfma_f32_32x32x16_bf16(b1, qr[d0], d0 == 0 ? negm : p1, 0, 0, 0); }
;     if constexpr (DQK == 96) {
; #pragma unroll
;         for (int d0 = 0; d0 < 2; ++d0) { const int ch = d0 * 2 + hi;
;             const bf16x8 b0 = *(const LAS bf16x8*)(buf + B_KR + swz32(r32, ch));
;             const bf16x8 b1 = *(const LAS bf16x8*)(buf + B_KR + swz32(32 + r32, ch));
;             p0 = __builtin_amdgcn_mfma_f32_32x32x16_bf16(b0, qr[4 + d0], p0, 0, 0, 0);
;             p1 = __builtin_amdgcn_mfma_f32_32x32x16_bf16(b1, qr[4 + d0], p1, 0, 0, 0); }
;     }
; }
; template <int D0> __device__ __forceinline__ void pv_one(f32x16& od, unsigned vb, bf16x8 pa0, bf16x8 pa1, bf16x8 pa2, bf16x8 pa3) {
;     const s16x4 l0 = tr_read<v_rd_off(D0, 0, 0)>(vb), h0 = tr_read<v_rd_off(D0, 0, 1)>(vb), l1 = tr_read<v_rd_off(D0, 1, 0)>(vb), h1 = tr_read<v_rd_off(D0, 1, 1)>(vb);
;     const s16x4 l2 = tr_read<v_rd_off(D0, 2, 0)>(vb), h2 = tr_read<v_rd_off(D0, 2, 1)>(vb), l3 = tr_read<v_rd_off(D0, 3, 0)>(vb), h3 = tr_read<v_rd_off(D0, 3, 1)>(vb);
;     asm volatile("s_waitcnt lgkmcnt(0)" ::: "memory"); SBAR();
.Lgqa_b_ld_done_0:
	s_waitcnt lgkmcnt(0)
	v_mfma_f32_32x32x16_bf16 v[34:49], v[224:227], v[156:159], v[34:49]
	s_waitcnt vmcnt(2)
	ds_write_b128 v187, v[130:133] offset:0
	ds_write_b128 v214, v[126:129] offset:12288
	v_exp_f32_e32 v143, v98
	v_exp_f32_e32 v145, v99
	v_mfma_f32_32x32x16_bf16 v[34:49], v[228:231], v[160:163], v[34:49]
	v_exp_f32_e32 v141, v100
	v_exp_f32_e32 v144, v101
	v_exp_f32_e32 v139, v102
	v_exp_f32_e32 v142, v103
	v_mfma_f32_32x32x16_bf16 v[34:49], v[232:235], v[82:85], v[34:49]
	v_exp_f32_e32 v138, v104
	v_exp_f32_e32 v140, v105
	v_exp_f32_e32 v151, v106
	v_exp_f32_e32 v153, v107
	v_exp_f32_e32 v149, v108
	v_mfma_f32_32x32x16_bf16 v[34:49], v[236:239], v[86:89], v[34:49]
	v_exp_f32_e32 v152, v109
	v_exp_f32_e32 v147, v110
	v_exp_f32_e32 v150, v111
	v_exp_f32_e32 v146, v112
	v_exp_f32_e32 v148, v113
	v_add_f32_e32 v154, v154, v155
	v_add_f32_e32 v136, v136, v154
	v_add_f32_e32 v164, v164, v165
	v_add_f32_e32 v136, v136, v164
	s_add_i32 s13, s13, 2
	s_addk_i32 s50, 0x80
	s_cmp_lt_u32 s8, s0
	s_cbranch_scc0 .Lgqa_exit_0
	s_waitcnt lgkmcnt(0)
	s_barrier
	ds_read_b128 v[224:227], v223 offset:0
	ds_read_b128 v[228:231], v223 offset:4096
	ds_read_b128 v[232:235], v252 offset:0
	ds_read_b128 v[236:239], v252 offset:4096
	ds_read_b128 v[240:243], v253 offset:0
	ds_read_b128 v[244:247], v253 offset:4096
	ds_read_b128 v[248:251], v2 offset:0
	v_exp_f32_e32 v66, v66
	v_exp_f32_e32 v67, v67
	v_exp_f32_e32 v68, v68
	v_exp_f32_e32 v69, v69
	v_exp_f32_e32 v70, v70
	v_exp_f32_e32 v71, v71
	v_exp_f32_e32 v72, v72
	v_exp_f32_e32 v73, v73
	s_waitcnt lgkmcnt(6)
	v_mfma_f32_32x32x16_bf16 v[98:113], v[224:227], v[114:117], v[18:33]
	ds_read_b128 v[224:227], v2 offset:4096
	v_exp_f32_e32 v74, v74
	v_exp_f32_e32 v75, v75
	v_exp_f32_e32 v76, v76
	v_cvt_pk_bf16_f32 v156, v143, v145
	v_cvt_pk_bf16_f32 v157, v141, v144
	v_add_f32_e32 v164, 0, v143
	v_add_f32_e32 v164, v145, v164
	v_add_f32_e32 v164, v141, v164
	s_waitcnt lgkmcnt(6)
	v_mfma_f32_32x32x16_bf16 v[82:97], v[228:231], v[114:117], v[18:33]
	v_exp_f32_e32 v77, v77
	v_exp_f32_e32 v78, v78
	v_exp_f32_e32 v79, v79
	v_cvt_pk_bf16_f32 v158, v139, v142
	v_cvt_pk_bf16_f32 v159, v138, v140
	v_add_f32_e32 v164, v144, v164
	v_add_f32_e32 v164, v139, v164
	v_add_f32_e32 v164, v142, v164
	s_waitcnt lgkmcnt(5)
	v_mfma_f32_32x32x16_bf16 v[98:113], v[232:235], v[12:15], v[98:113]
	v_exp_f32_e32 v80, v80
	v_exp_f32_e32 v81, v81
	v_cvt_pk_bf16_f32 v160, v151, v153
	v_cvt_pk_bf16_f32 v161, v149, v152
	v_cvt_pk_bf16_f32 v162, v147, v150
	v_cvt_pk_bf16_f32 v163, v146, v148
	v_add_f32_e32 v164, v138, v164
	v_add_f32_e32 v164, v140, v164
	v_add_f32_e32 v164, v151, v164
	s_waitcnt lgkmcnt(4)
	v_mfma_f32_32x32x16_bf16 v[82:97], v[236:239], v[12:15], v[82:97]
	v_add_f32_e32 v164, v153, v164
	v_add_f32_e32 v164, v149, v164
	v_add_f32_e32 v164, v152, v164
	v_add_f32_e32 v164, v147, v164
	v_add_f32_e32 v164, v150, v164
	v_add_f32_e32 v164, v146, v164
	v_add_f32_e32 v164, v148, v164
	s_waitcnt lgkmcnt(3)
	v_mfma_f32_32x32x16_bf16 v[98:113], v[240:243], v[8:11], v[98:113]
	ds_read_b64_tr_b16 v[138:139], v213 offset:40960
	ds_read_b64_tr_b16 v[140:141], v213 offset:41984
	ds_read_b64_tr_b16 v[142:143], v213 offset:43008
	ds_read_b64_tr_b16 v[144:145], v213 offset:44032
	v_add_f32_e32 v164, v66, v164
	v_add_f32_e32 v164, v67, v164
	v_add_f32_e32 v164, v68, v164
	v_add_f32_e32 v164, v69, v164
	s_waitcnt lgkmcnt(6)
	v_mfma_f32_32x32x16_bf16 v[82:97], v[244:247], v[8:11], v[82:97]
	ds_read_b64_tr_b16 v[146:147], v213 offset:45056
	ds_read_b64_tr_b16 v[148:149], v213 offset:46080
	ds_read_b64_tr_b16 v[150:151], v213 offset:47104
	ds_read_b64_tr_b16 v[152:153], v213 offset:48128
	v_add_f32_e32 v164, v70, v164
	v_add_f32_e32 v164, v71, v164
	v_add_f32_e32 v164, v72, v164
	v_add_f32_e32 v164, v73, v164
	s_waitcnt lgkmcnt(9)
	v_mfma_f32_32x32x16_bf16 v[98:113], v[248:251], v[4:7], v[98:113]
	v_add_f32_e32 v164, v74, v164
	v_add_f32_e32 v164, v75, v164
	v_add_f32_e32 v164, v76, v164
	v_add_f32_e32 v164, v77, v164
	s_waitcnt lgkmcnt(8)
	v_mfma_f32_32x32x16_bf16 v[82:97], v[224:227], v[4:7], v[82:97]
	ds_read_b64_tr_b16 v[224:225], v213 offset:41472
	ds_read_b64_tr_b16 v[226:227], v213 offset:42496
	ds_read_b64_tr_b16 v[228:229], v213 offset:43520
	ds_read_b64_tr_b16 v[230:231], v213 offset:44544
	ds_read_b64_tr_b16 v[232:233], v213 offset:45568
	ds_read_b64_tr_b16 v[234:235], v213 offset:46592
	ds_read_b64_tr_b16 v[236:237], v213 offset:47616
	ds_read_b64_tr_b16 v[238:239], v213 offset:48640
	s_waitcnt lgkmcnt(8)
	v_mfma_f32_32x32x16_bf16 v[50:65], v[138:141], v[156:159], v[50:65]
	v_add_f32_e32 v164, v78, v164
	v_add_f32_e32 v164, v79, v164
	v_add_f32_e32 v164, v80, v164
	v_add_f32_e32 v154, v81, v164
	v_mov_b32_e32 v155, v154
	v_mfma_f32_32x32x16_bf16 v[50:65], v[142:145], v[160:163], v[50:65]
	v_cvt_pk_bf16_f32 v66, v66, v67
	v_cvt_pk_bf16_f32 v67, v68, v69
	v_cvt_pk_bf16_f32 v68, v70, v71
	v_cvt_pk_bf16_f32 v69, v72, v73
	v_cvt_pk_bf16_f32 v70, v74, v75
	v_cvt_pk_bf16_f32 v71, v76, v77
	v_cvt_pk_bf16_f32 v72, v78, v79
	v_cvt_pk_bf16_f32 v73, v80, v81
	v_permlane32_swap_b32_e32 v154, v155
	v_mfma_f32_32x32x16_bf16 v[50:65], v[146:149], v[66:69], v[50:65]
	s_add_i32 s8, s13, -1
	s_cmp_lt_u32 s8, s31
	s_cselect_b32 s9, 0, s31
	s_cselect_b32 s35, s12, s29
	s_lshl_b32 s9, s9, 6
	s_sub_i32 s9, s35, s9
	s_add_i32 s52, s9, s50
	s_ashr_i32 s53, s52, 31
	s_lshl_b64 s[52:53], s[52:53], 8
	s_add_u32 s54, s42, s52
	v_mfma_f32_32x32x16_bf16 v[50:65], v[150:153], v[70:73], v[50:65]
	s_addc_u32 s55, s43, s53
	s_add_u32 s56, s44, s52
	s_addc_u32 s57, s45, s53
	global_load_dwordx4 v[130:133], v137, s[54:55]
	global_load_dwordx4 v[126:129], v137, s[56:57]
	s_waitcnt lgkmcnt(0)
	v_mfma_f32_32x32x16_bf16 v[34:49], v[224:227], v[156:159], v[34:49]
	s_waitcnt vmcnt(2)
	ds_write_b128 v187, v[118:121] offset:20480
	ds_write_b128 v214, v[122:125] offset:32768
	v_exp_f32_e32 v168, v98
	v_exp_f32_e32 v169, v99
	v_mfma_f32_32x32x16_bf16 v[34:49], v[228:231], v[160:163], v[34:49]
	v_exp_f32_e32 v170, v100
	v_exp_f32_e32 v171, v101
	v_exp_f32_e32 v172, v102
	v_exp_f32_e32 v173, v103
	v_mfma_f32_32x32x16_bf16 v[34:49], v[232:235], v[66:69], v[34:49]
	v_exp_f32_e32 v174, v104
	v_exp_f32_e32 v175, v105
	v_exp_f32_e32 v176, v106
	v_exp_f32_e32 v177, v107
	v_exp_f32_e32 v178, v108
	v_mfma_f32_32x32x16_bf16 v[34:49], v[236:239], v[70:73], v[34:49]
	v_exp_f32_e32 v179, v109
	v_exp_f32_e32 v180, v110
	v_exp_f32_e32 v181, v111
	v_exp_f32_e32 v182, v112
	v_exp_f32_e32 v183, v113
	s_waitcnt lgkmcnt(0)
	s_barrier
; __device__ __forceinline__ void finishSM(f32x16& p0, f32x16& p1, float alpha, float& l_reg, bf16x8& pa0, bf16x8& pa1, bf16x8& pa2, bf16x8& pa3) {
; #pragma unroll
;     for (int r = 0; r < 16; ++r) p1[r] = EXP_PROBE ? fmaf(p1[r], 0.001f, 1.f) : __builtin_amdgcn_exp2f(p1[r]);
;     float ps = 0.f;
; #pragma unroll
;     for (int r = 0; r < 16; ++r) ps += p0[r];
; #pragma unroll
;     for (int r = 0; r < 16; ++r) ps += p1[r];
;     { auto rr = __builtin_amdgcn_permlane32_swap(__float_as_uint(ps), __float_as_uint(ps), false, false);
;       ps = __uint_as_float(rr[0]) + __uint_as_float(rr[1]); }
;     l_reg = l_reg * alpha + ps;
;     ATT_PKN(p0, 0, pa0); ATT_PKN(p0, 8, pa1); ATT_PKN(p1, 0, pa2); ATT_PKN(p1, 8, pa3);
; }
; template <int DQK> __device__ __forceinline__ void qkt(f32x16& p0, f32x16& p1, const LAS char* buf, const bf16x8* qr, int r32, int hi, const f32x16& negm) {
; #pragma unroll
;     for (int d0 = 0; d0 < 4; ++d0) { const int ch = d0 * 2 + hi;
;         const bf16x8 b0 = *(const LAS bf16x8*)(buf + B_KN + swz64(r32, ch));
;         const bf16x8 b1 = *(const LAS bf16x8*)(buf + B_KN + swz64(32 + r32, ch));
;         p0 = __builtin_amdgcn_mfma_f32_32x32x16_bf16(b0, qr[d0], d0 == 0 ? negm : p0, 0, 0, 0);
;         p1 = __builtin_amdgcn_mfma_f32_32x32x16_bf16(b1, qr[d0], d0 == 0 ? negm : p1, 0, 0, 0); }
;     if constexpr (DQK == 96) {
; #pragma unroll
;         for (int d0 = 0; d0 < 2; ++d0) { const int ch = d0 * 2 + hi;
;             const bf16x8 b0 = *(const LAS bf16x8*)(buf + B_KR + swz32(r32, ch));
;             const bf16x8 b1 = *(const LAS bf16x8*)(buf + B_KR + swz32(32 + r32, ch));
;             p0 = __builtin_amdgcn_mfma_f32_32x32x16_bf16(b0, qr[4 + d0], p0, 0, 0, 0);
;             p1 = __builtin_amdgcn_mfma_f32_32x32x16_bf16(b1, qr[4 + d0], p1, 0, 0, 0); }
;     }
; }
; template <int D0> __device__ __forceinline__ void pv_one(f32x16& od, unsigned vb, bf16x8 pa0, bf16x8 pa1, bf16x8 pa2, bf16x8 pa3) {
;     const s16x4 l0 = tr_read<v_rd_off(D0, 0, 0)>(vb), h0 = tr_read<v_rd_off(D0, 0, 1)>(vb), l1 = tr_read<v_rd_off(D0, 1, 0)>(vb), h1 = tr_read<v_rd_off(D0, 1, 1)>(vb);
;     const s16x4 l2 = tr_read<v_rd_off(D0, 2, 0)>(vb), h2 = tr_read<v_rd_off(D0, 2, 1)>(vb), l3 = tr_read<v_rd_off(D0, 3, 0)>(vb), h3 = tr_read<v_rd_off(D0, 3, 1)>(vb);
;     asm volatile("s_waitcnt lgkmcnt(0)" ::: "memory"); SBAR();
	ds_read_b128 v[224:227], v223 offset:20480
	ds_read_b128 v[228:231], v223 offset:24576
	ds_read_b128 v[232:235], v252 offset:20480
	ds_read_b128 v[236:239], v252 offset:24576
	ds_read_b128 v[240:243], v253 offset:20480
	ds_read_b128 v[244:247], v253 offset:24576
	ds_read_b128 v[248:251], v2 offset:20480
	v_exp_f32_e32 v82, v82
	v_exp_f32_e32 v83, v83
	v_exp_f32_e32 v84, v84
	v_exp_f32_e32 v85, v85
	v_exp_f32_e32 v86, v86
	v_exp_f32_e32 v87, v87
	v_exp_f32_e32 v88, v88
	v_exp_f32_e32 v89, v89
	s_waitcnt lgkmcnt(6)
	v_mfma_f32_32x32x16_bf16 v[98:113], v[224:227], v[114:117], v[18:33]
	ds_read_b128 v[224:227], v2 offset:24576
	v_exp_f32_e32 v90, v90
	v_exp_f32_e32 v91, v91
	v_exp_f32_e32 v92, v92
	v_cvt_pk_bf16_f32 v156, v168, v169
	v_cvt_pk_bf16_f32 v157, v170, v171
	v_add_f32_e32 v164, 0, v168
	v_add_f32_e32 v164, v169, v164
	v_add_f32_e32 v164, v170, v164
	s_waitcnt lgkmcnt(6)
	v_mfma_f32_32x32x16_bf16 v[66:81], v[228:231], v[114:117], v[18:33]
	v_exp_f32_e32 v93, v93
	v_exp_f32_e32 v94, v94
	v_exp_f32_e32 v95, v95
	v_cvt_pk_bf16_f32 v158, v172, v173
	v_cvt_pk_bf16_f32 v159, v174, v175
	v_add_f32_e32 v164, v171, v164
	v_add_f32_e32 v164, v172, v164
	v_add_f32_e32 v164, v173, v164
	s_waitcnt lgkmcnt(5)
	v_mfma_f32_32x32x16_bf16 v[98:113], v[232:235], v[12:15], v[98:113]
	v_exp_f32_e32 v96, v96
	v_exp_f32_e32 v97, v97
	v_cvt_pk_bf16_f32 v160, v176, v177
	v_cvt_pk_bf16_f32 v161, v178, v179
	v_cvt_pk_bf16_f32 v162, v180, v181
	v_cvt_pk_bf16_f32 v163, v182, v183
	v_add_f32_e32 v164, v174, v164
	v_add_f32_e32 v164, v175, v164
	v_add_f32_e32 v164, v176, v164
	s_waitcnt lgkmcnt(4)
	v_mfma_f32_32x32x16_bf16 v[66:81], v[236:239], v[12:15], v[66:81]
	v_add_f32_e32 v164, v177, v164
	v_add_f32_e32 v164, v178, v164
	v_add_f32_e32 v164, v179, v164
	v_add_f32_e32 v164, v180, v164
	v_add_f32_e32 v164, v181, v164
	v_add_f32_e32 v164, v182, v164
	v_add_f32_e32 v164, v183, v164
	s_waitcnt lgkmcnt(3)
	v_mfma_f32_32x32x16_bf16 v[98:113], v[240:243], v[8:11], v[98:113]
	ds_read_b64_tr_b16 v[168:169], v213 offset:0
	ds_read_b64_tr_b16 v[170:171], v213 offset:1024
	ds_read_b64_tr_b16 v[172:173], v213 offset:2048
	ds_read_b64_tr_b16 v[174:175], v213 offset:3072
	v_add_f32_e32 v164, v82, v164
	v_add_f32_e32 v164, v83, v164
	v_add_f32_e32 v164, v84, v164
	v_add_f32_e32 v164, v85, v164
	s_waitcnt lgkmcnt(6)
	v_mfma_f32_32x32x16_bf16 v[66:81], v[244:247], v[8:11], v[66:81]
	ds_read_b64_tr_b16 v[176:177], v213 offset:4096
	ds_read_b64_tr_b16 v[178:179], v213 offset:5120
	ds_read_b64_tr_b16 v[180:181], v213 offset:6144
	ds_read_b64_tr_b16 v[182:183], v213 offset:7168
	v_add_f32_e32 v164, v86, v164
	v_add_f32_e32 v164, v87, v164
	v_add_f32_e32 v164, v88, v164
	v_add_f32_e32 v164, v89, v164
	s_waitcnt lgkmcnt(9)
	v_mfma_f32_32x32x16_bf16 v[98:113], v[248:251], v[4:7], v[98:113]
	v_add_f32_e32 v164, v90, v164
	v_add_f32_e32 v164, v91, v164
	v_add_f32_e32 v164, v92, v164
	v_add_f32_e32 v164, v93, v164
	s_waitcnt lgkmcnt(8)
	v_mfma_f32_32x32x16_bf16 v[66:81], v[224:227], v[4:7], v[66:81]
	ds_read_b64_tr_b16 v[224:225], v213 offset:512
	ds_read_b64_tr_b16 v[226:227], v213 offset:1536
	ds_read_b64_tr_b16 v[228:229], v213 offset:2560
	ds_read_b64_tr_b16 v[230:231], v213 offset:3584
	ds_read_b64_tr_b16 v[232:233], v213 offset:4608
	ds_read_b64_tr_b16 v[234:235], v213 offset:5632
	ds_read_b64_tr_b16 v[236:237], v213 offset:6656
	ds_read_b64_tr_b16 v[238:239], v213 offset:7680
	s_waitcnt lgkmcnt(8)
	v_mfma_f32_32x32x16_bf16 v[50:65], v[168:171], v[156:159], v[50:65]
	v_add_f32_e32 v164, v94, v164
	v_add_f32_e32 v164, v95, v164
	v_add_f32_e32 v164, v96, v164
	v_add_f32_e32 v164, v97, v164
	v_mov_b32_e32 v165, v164
	v_mfma_f32_32x32x16_bf16 v[50:65], v[172:175], v[160:163], v[50:65]
	v_cvt_pk_bf16_f32 v82, v82, v83
	v_cvt_pk_bf16_f32 v83, v84, v85
	v_cvt_pk_bf16_f32 v84, v86, v87
	v_cvt_pk_bf16_f32 v85, v88, v89
	v_cvt_pk_bf16_f32 v86, v90, v91
	v_cvt_pk_bf16_f32 v87, v92, v93
	v_cvt_pk_bf16_f32 v88, v94, v95
	v_cvt_pk_bf16_f32 v89, v96, v97
	v_permlane32_swap_b32_e32 v164, v165
	v_mfma_f32_32x32x16_bf16 v[50:65], v[176:179], v[82:85], v[50:65]
	v_mfma_f32_32x32x16_bf16 v[50:65], v[180:183], v[86:89], v[50:65]
	s_cmp_ge_u32 s13, s30
	s_cbranch_scc1 .Lgqa_b_noload_1
	s_cmp_lt_u32 s13, s31
	s_cselect_b32 s9, 0, s31
	s_cselect_b32 s35, s12, s29
	s_lshl_b32 s9, s9, 6
	s_sub_i32 s9, s35, s9
	s_add_i32 s52, s9, s50
	s_add_i32 s52, s52, 64
	s_ashr_i32 s53, s52, 31
	s_lshl_b64 s[52:53], s[52:53], 8
	s_add_u32 s54, s42, s52
	s_addc_u32 s55, s43, s53
	s_add_u32 s56, s44, s52
	s_addc_u32 s57, s45, s53
	global_load_dwordx4 v[118:121], v137, s[54:55]
	global_load_dwordx4 v[122:125], v137, s[56:57]
; __device__ __forceinline__ void finishSM(f32x16& p0, f32x16& p1, float alpha, float& l_reg, bf16x8& pa0, bf16x8& pa1, bf16x8& pa2, bf16x8& pa3) {
; #pragma unroll
;     for (int r = 0; r < 16; ++r) p1[r] = EXP_PROBE ? fmaf(p1[r], 0.001f, 1.f) : __builtin_amdgcn_exp2f(p1[r]);
;     float ps = 0.f;
; #pragma unroll
;     for (int r = 0; r < 16; ++r) ps += p0[r];
; #pragma unroll
;     for (int r = 0; r < 16; ++r) ps += p1[r];
;     { auto rr = __builtin_amdgcn_permlane32_swap(__float_as_uint(ps), __float_as_uint(ps), false, false);
;       ps = __uint_as_float(rr[0]) + __uint_as_float(rr[1]); }
;     l_reg = l_reg * alpha + ps;
;     ATT_PKN(p0, 0, pa0); ATT_PKN(p0, 8, pa1); ATT_PKN(p1, 0, pa2); ATT_PKN(p1, 8, pa3);
; }
; template <int DQK> __device__ __forceinline__ void qkt(f32x16& p0, f32x16& p1, const LAS char* buf, const bf16x8* qr, int r32, int hi, const f32x16& negm) {
; #pragma unroll
;     for (int d0 = 0; d0 < 4; ++d0) { const int ch = d0 * 2 + hi;
;         const bf16x8 b0 = *(const LAS bf16x8*)(buf + B_KN + swz64(r32, ch));
;         const bf16x8 b1 = *(const LAS bf16x8*)(buf + B_KN + swz64(32 + r32, ch));
;         p0 = __builtin_amdgcn_mfma_f32_32x32x16_bf16(b0, qr[d0], d0 == 0 ? negm : p0, 0, 0, 0);
;         p1 = __builtin_amdgcn_mfma_f32_32x32x16_bf16(b1, qr[d0], d0 == 0 ? negm : p1, 0, 0, 0); }
;     if constexpr (DQK == 96) {
; #pragma unroll
;         for (int d0 = 0; d0 < 2; ++d0) { const int ch = d0 * 2 + hi;
;             const bf16x8 b0 = *(const LAS bf16x8*)(buf + B_KR + swz32(r32, ch));
;             const bf16x8 b1 = *(const LAS bf16x8*)(buf + B_KR + swz32(32 + r32, ch));
;             p0 = __builtin_amdgcn_mfma_f32_32x32x16_bf16(b0, qr[4 + d0], p0, 0, 0, 0);
;             p1 = __builtin_amdgcn_mfma_f32_32x32x16_bf16(b1, qr[4 + d0], p1, 0, 0, 0); }
;     }
; }
; template <int D0> __device__ __forceinline__ void pv_one(f32x16& od, unsigned vb, bf16x8 pa0, bf16x8 pa1, bf16x8 pa2, bf16x8 pa3) {
;     const s16x4 l0 = tr_read<v_rd_off(D0, 0, 0)>(vb), h0 = tr_read<v_rd_off(D0, 0, 1)>(vb), l1 = tr_read<v_rd_off(D0, 1, 0)>(vb), h1 = tr_read<v_rd_off(D0, 1, 1)>(vb);
;     const s16x4 l2 = tr_read<v_rd_off(D0, 2, 0)>(vb), h2 = tr_read<v_rd_off(D0, 2, 1)>(vb), l3 = tr_read<v_rd_off(D0, 3, 0)>(vb), h3 = tr_read<v_rd_off(D0, 3, 1)>(vb);
;     asm volatile("s_waitcnt lgkmcnt(0)" ::: "memory"); SBAR();
.Lgqa_b_ld_done_1:
	s_waitcnt lgkmcnt(0)
	v_mfma_f32_32x32x16_bf16 v[34:49], v[224:227], v[156:159], v[34:49]
	s_waitcnt vmcnt(2)
	ds_write_b128 v187, v[130:133] offset:40960
	ds_write_b128 v214, v[126:129] offset:53248
	v_exp_f32_e32 v143, v98
	v_exp_f32_e32 v145, v99
	v_mfma_f32_32x32x16_bf16 v[34:49], v[228:231], v[160:163], v[34:49]
	v_exp_f32_e32 v141, v100
	v_exp_f32_e32 v144, v101
	v_exp_f32_e32 v139, v102
	v_exp_f32_e32 v142, v103
	v_mfma_f32_32x32x16_bf16 v[34:49], v[232:235], v[82:85], v[34:49]
	v_exp_f32_e32 v138, v104
	v_exp_f32_e32 v140, v105
	v_exp_f32_e32 v151, v106
	v_exp_f32_e32 v153, v107
	v_exp_f32_e32 v149, v108
	v_mfma_f32_32x32x16_bf16 v[34:49], v[236:239], v[86:89], v[34:49]
	v_exp_f32_e32 v152, v109
	v_exp_f32_e32 v147, v110
	v_exp_f32_e32 v150, v111
	v_exp_f32_e32 v146, v112
	v_exp_f32_e32 v148, v113
	v_add_f32_e32 v154, v154, v155
	v_add_f32_e32 v136, v136, v154
	v_add_f32_e32 v164, v164, v165
	v_add_f32_e32 v136, v136, v164
	s_add_i32 s13, s13, 2
	s_addk_i32 s50, 0x80
	s_cmp_lt_u32 s8, s0
	s_cbranch_scc0 .Lgqa_exit_1
	s_waitcnt lgkmcnt(0)
	s_barrier
	ds_read_b128 v[224:227], v223 offset:40960
	ds_read_b128 v[228:231], v223 offset:45056
	ds_read_b128 v[232:235], v252 offset:40960
	ds_read_b128 v[236:239], v252 offset:45056
	ds_read_b128 v[240:243], v253 offset:40960
	ds_read_b128 v[244:247], v253 offset:45056
	ds_read_b128 v[248:251], v2 offset:40960
	v_exp_f32_e32 v66, v66
	v_exp_f32_e32 v67, v67
	v_exp_f32_e32 v68, v68
	v_exp_f32_e32 v69, v69
	v_exp_f32_e32 v70, v70
	v_exp_f32_e32 v71, v71
	v_exp_f32_e32 v72, v72
	v_exp_f32_e32 v73, v73
	s_waitcnt lgkmcnt(6)
	v_mfma_f32_32x32x16_bf16 v[98:113], v[224:227], v[114:117], v[18:33]
	ds_read_b128 v[224:227], v2 offset:45056
	v_exp_f32_e32 v74, v74
	v_exp_f32_e32 v75, v75
	v_exp_f32_e32 v76, v76
	v_cvt_pk_bf16_f32 v156, v143, v145
	v_cvt_pk_bf16_f32 v157, v141, v144
	v_add_f32_e32 v164, 0, v143
	v_add_f32_e32 v164, v145, v164
	v_add_f32_e32 v164, v141, v164
	s_waitcnt lgkmcnt(6)
	v_mfma_f32_32x32x16_bf16 v[82:97], v[228:231], v[114:117], v[18:33]
	v_exp_f32_e32 v77, v77
	v_exp_f32_e32 v78, v78
	v_exp_f32_e32 v79, v79
	v_cvt_pk_bf16_f32 v158, v139, v142
	v_cvt_pk_bf16_f32 v159, v138, v140
	v_add_f32_e32 v164, v144, v164
	v_add_f32_e32 v164, v139, v164
	v_add_f32_e32 v164, v142, v164
	s_waitcnt lgkmcnt(5)
	v_mfma_f32_32x32x16_bf16 v[98:113], v[232:235], v[12:15], v[98:113]
	v_exp_f32_e32 v80, v80
	v_exp_f32_e32 v81, v81
	v_cvt_pk_bf16_f32 v160, v151, v153
	v_cvt_pk_bf16_f32 v161, v149, v152
	v_cvt_pk_bf16_f32 v162, v147, v150
	v_cvt_pk_bf16_f32 v163, v146, v148
	v_add_f32_e32 v164, v138, v164
	v_add_f32_e32 v164, v140, v164
	v_add_f32_e32 v164, v151, v164
	s_waitcnt lgkmcnt(4)
	v_mfma_f32_32x32x16_bf16 v[82:97], v[236:239], v[12:15], v[82:97]
	v_add_f32_e32 v164, v153, v164
	v_add_f32_e32 v164, v149, v164
	v_add_f32_e32 v164, v152, v164
	v_add_f32_e32 v164, v147, v164
	v_add_f32_e32 v164, v150, v164
	v_add_f32_e32 v164, v146, v164
	v_add_f32_e32 v164, v148, v164
	s_waitcnt lgkmcnt(3)
	v_mfma_f32_32x32x16_bf16 v[98:113], v[240:243], v[8:11], v[98:113]
	ds_read_b64_tr_b16 v[138:139], v213 offset:20480
	ds_read_b64_tr_b16 v[140:141], v213 offset:21504
	ds_read_b64_tr_b16 v[142:143], v213 offset:22528
	ds_read_b64_tr_b16 v[144:145], v213 offset:23552
	v_add_f32_e32 v164, v66, v164
	v_add_f32_e32 v164, v67, v164
	v_add_f32_e32 v164, v68, v164
	v_add_f32_e32 v164, v69, v164
	s_waitcnt lgkmcnt(6)
	v_mfma_f32_32x32x16_bf16 v[82:97], v[244:247], v[8:11], v[82:97]
	ds_read_b64_tr_b16 v[146:147], v213 offset:24576
	ds_read_b64_tr_b16 v[148:149], v213 offset:25600
	ds_read_b64_tr_b16 v[150:151], v213 offset:26624
	ds_read_b64_tr_b16 v[152:153], v213 offset:27648
	v_add_f32_e32 v164, v70, v164
	v_add_f32_e32 v164, v71, v164
	v_add_f32_e32 v164, v72, v164
	v_add_f32_e32 v164, v73, v164
	s_waitcnt lgkmcnt(9)
	v_mfma_f32_32x32x16_bf16 v[98:113], v[248:251], v[4:7], v[98:113]
	v_add_f32_e32 v164, v74, v164
	v_add_f32_e32 v164, v75, v164
	v_add_f32_e32 v164, v76, v164
	v_add_f32_e32 v164, v77, v164
	s_waitcnt lgkmcnt(8)
	v_mfma_f32_32x32x16_bf16 v[82:97], v[224:227], v[4:7], v[82:97]
	ds_read_b64_tr_b16 v[224:225], v213 offset:20992
	ds_read_b64_tr_b16 v[226:227], v213 offset:22016
	ds_read_b64_tr_b16 v[228:229], v213 offset:23040
	ds_read_b64_tr_b16 v[230:231], v213 offset:24064
	ds_read_b64_tr_b16 v[232:233], v213 offset:25088
	ds_read_b64_tr_b16 v[234:235], v213 offset:26112
	ds_read_b64_tr_b16 v[236:237], v213 offset:27136
	ds_read_b64_tr_b16 v[238:239], v213 offset:28160
	s_waitcnt lgkmcnt(8)
	v_mfma_f32_32x32x16_bf16 v[50:65], v[138:141], v[156:159], v[50:65]
	v_add_f32_e32 v164, v78, v164
	v_add_f32_e32 v164, v79, v164
	v_add_f32_e32 v164, v80, v164
	v_add_f32_e32 v154, v81, v164
	v_mov_b32_e32 v155, v154
	v_mfma_f32_32x32x16_bf16 v[50:65], v[142:145], v[160:163], v[50:65]
	v_cvt_pk_bf16_f32 v66, v66, v67
	v_cvt_pk_bf16_f32 v67, v68, v69
	v_cvt_pk_bf16_f32 v68, v70, v71
	v_cvt_pk_bf16_f32 v69, v72, v73
	v_cvt_pk_bf16_f32 v70, v74, v75
	v_cvt_pk_bf16_f32 v71, v76, v77
	v_cvt_pk_bf16_f32 v72, v78, v79
	v_cvt_pk_bf16_f32 v73, v80, v81
	v_permlane32_swap_b32_e32 v154, v155
	v_mfma_f32_32x32x16_bf16 v[50:65], v[146:149], v[66:69], v[50:65]
	s_add_i32 s8, s13, -1
	s_cmp_lt_u32 s8, s31
	s_cselect_b32 s9, 0, s31
	s_cselect_b32 s35, s12, s29
	s_lshl_b32 s9, s9, 6
	s_sub_i32 s9, s35, s9
	s_add_i32 s52, s9, s50
	s_ashr_i32 s53, s52, 31
	s_lshl_b64 s[52:53], s[52:53], 8
	s_add_u32 s54, s42, s52
	v_mfma_f32_32x32x16_bf16 v[50:65], v[150:153], v[70:73], v[50:65]
	s_addc_u32 s55, s43, s53
	s_add_u32 s56, s44, s52
	s_addc_u32 s57, s45, s53
	global_load_dwordx4 v[130:133], v137, s[54:55]
	global_load_dwordx4 v[126:129], v137, s[56:57]
	s_waitcnt lgkmcnt(0)
	v_mfma_f32_32x32x16_bf16 v[34:49], v[224:227], v[156:159], v[34:49]
	s_waitcnt vmcnt(2)
	ds_write_b128 v187, v[118:121] offset:0
	ds_write_b128 v214, v[122:125] offset:12288
	v_exp_f32_e32 v168, v98
	v_exp_f32_e32 v169, v99
	v_mfma_f32_32x32x16_bf16 v[34:49], v[228:231], v[160:163], v[34:49]
	v_exp_f32_e32 v170, v100
	v_exp_f32_e32 v171, v101
	v_exp_f32_e32 v172, v102
	v_exp_f32_e32 v173, v103
	v_mfma_f32_32x32x16_bf16 v[34:49], v[232:235], v[66:69], v[34:49]
	v_exp_f32_e32 v174, v104
	v_exp_f32_e32 v175, v105
	v_exp_f32_e32 v176, v106
	v_exp_f32_e32 v177, v107
	v_exp_f32_e32 v178, v108
	v_mfma_f32_32x32x16_bf16 v[34:49], v[236:239], v[70:73], v[34:49]
	v_exp_f32_e32 v179, v109
	v_exp_f32_e32 v180, v110
	v_exp_f32_e32 v181, v111
	v_exp_f32_e32 v182, v112
	v_exp_f32_e32 v183, v113
	s_waitcnt lgkmcnt(0)
	s_barrier
; __device__ __forceinline__ void finishSM(f32x16& p0, f32x16& p1, float alpha, float& l_reg, bf16x8& pa0, bf16x8& pa1, bf16x8& pa2, bf16x8& pa3) {
; #pragma unroll
;     for (int r = 0; r < 16; ++r) p1[r] = EXP_PROBE ? fmaf(p1[r], 0.001f, 1.f) : __builtin_amdgcn_exp2f(p1[r]);
;     float ps = 0.f;
; #pragma unroll
;     for (int r = 0; r < 16; ++r) ps += p0[r];
; #pragma unroll
;     for (int r = 0; r < 16; ++r) ps += p1[r];
;     { auto rr = __builtin_amdgcn_permlane32_swap(__float_as_uint(ps), __float_as_uint(ps), false, false);
;       ps = __uint_as_float(rr[0]) + __uint_as_float(rr[1]); }
;     l_reg = l_reg * alpha + ps;
;     ATT_PKN(p0, 0, pa0); ATT_PKN(p0, 8, pa1); ATT_PKN(p1, 0, pa2); ATT_PKN(p1, 8, pa3);
; }
; template <int DQK> __device__ __forceinline__ void qkt(f32x16& p0, f32x16& p1, const LAS char* buf, const bf16x8* qr, int r32, int hi, const f32x16& negm) {
; #pragma unroll
;     for (int d0 = 0; d0 < 4; ++d0) { const int ch = d0 * 2 + hi;
;         const bf16x8 b0 = *(const LAS bf16x8*)(buf + B_KN + swz64(r32, ch));
;         const bf16x8 b1 = *(const LAS bf16x8*)(buf + B_KN + swz64(32 + r32, ch));
;         p0 = __builtin_amdgcn_mfma_f32_32x32x16_bf16(b0, qr[d0], d0 == 0 ? negm : p0, 0, 0, 0);
;         p1 = __builtin_amdgcn_mfma_f32_32x32x16_bf16(b1, qr[d0], d0 == 0 ? negm : p1, 0, 0, 0); }
;     if constexpr (DQK == 96) {
; #pragma unroll
;         for (int d0 = 0; d0 < 2; ++d0) { const int ch = d0 * 2 + hi;
;             const bf16x8 b0 = *(const LAS bf16x8*)(buf + B_KR + swz32(r32, ch));
;             const bf16x8 b1 = *(const LAS bf16x8*)(buf + B_KR + swz32(32 + r32, ch));
;             p0 = __builtin_amdgcn_mfma_f32_32x32x16_bf16(b0, qr[4 + d0], p0, 0, 0, 0);
;             p1 = __builtin_amdgcn_mfma_f32_32x32x16_bf16(b1, qr[4 + d0], p1, 0, 0, 0); }
;     }
; }
; template <int D0> __device__ __forceinline__ void pv_one(f32x16& od, unsigned vb, bf16x8 pa0, bf16x8 pa1, bf16x8 pa2, bf16x8 pa3) {
;     const s16x4 l0 = tr_read<v_rd_off(D0, 0, 0)>(vb), h0 = tr_read<v_rd_off(D0, 0, 1)>(vb), l1 = tr_read<v_rd_off(D0, 1, 0)>(vb), h1 = tr_read<v_rd_off(D0, 1, 1)>(vb);
;     const s16x4 l2 = tr_read<v_rd_off(D0, 2, 0)>(vb), h2 = tr_read<v_rd_off(D0, 2, 1)>(vb), l3 = tr_read<v_rd_off(D0, 3, 0)>(vb), h3 = tr_read<v_rd_off(D0, 3, 1)>(vb);
;     asm volatile("s_waitcnt lgkmcnt(0)" ::: "memory"); SBAR();
	ds_read_b128 v[224:227], v223 offset:0
	ds_read_b128 v[228:231], v223 offset:4096
	ds_read_b128 v[232:235], v252 offset:0
	ds_read_b128 v[236:239], v252 offset:4096
	ds_read_b128 v[240:243], v253 offset:0
	ds_read_b128 v[244:247], v253 offset:4096
	ds_read_b128 v[248:251], v2 offset:0
	v_exp_f32_e32 v82, v82
	v_exp_f32_e32 v83, v83
	v_exp_f32_e32 v84, v84
	v_exp_f32_e32 v85, v85
	v_exp_f32_e32 v86, v86
	v_exp_f32_e32 v87, v87
	v_exp_f32_e32 v88, v88
	v_exp_f32_e32 v89, v89
	s_waitcnt lgkmcnt(6)
	v_mfma_f32_32x32x16_bf16 v[98:113], v[224:227], v[114:117], v[18:33]
	ds_read_b128 v[224:227], v2 offset:4096
	v_exp_f32_e32 v90, v90
	v_exp_f32_e32 v91, v91
	v_exp_f32_e32 v92, v92
	v_cvt_pk_bf16_f32 v156, v168, v169
	v_cvt_pk_bf16_f32 v157, v170, v171
	v_add_f32_e32 v164, 0, v168
	v_add_f32_e32 v164, v169, v164
	v_add_f32_e32 v164, v170, v164
	s_waitcnt lgkmcnt(6)
	v_mfma_f32_32x32x16_bf16 v[66:81], v[228:231], v[114:117], v[18:33]
	v_exp_f32_e32 v93, v93
	v_exp_f32_e32 v94, v94
	v_exp_f32_e32 v95, v95
	v_cvt_pk_bf16_f32 v158, v172, v173
	v_cvt_pk_bf16_f32 v159, v174, v175
	v_add_f32_e32 v164, v171, v164
	v_add_f32_e32 v164, v172, v164
	v_add_f32_e32 v164, v173, v164
	s_waitcnt lgkmcnt(5)
	v_mfma_f32_32x32x16_bf16 v[98:113], v[232:235], v[12:15], v[98:113]
	v_exp_f32_e32 v96, v96
	v_exp_f32_e32 v97, v97
	v_cvt_pk_bf16_f32 v160, v176, v177
	v_cvt_pk_bf16_f32 v161, v178, v179
	v_cvt_pk_bf16_f32 v162, v180, v181
	v_cvt_pk_bf16_f32 v163, v182, v183
	v_add_f32_e32 v164, v174, v164
	v_add_f32_e32 v164, v175, v164
	v_add_f32_e32 v164, v176, v164
	s_waitcnt lgkmcnt(4)
	v_mfma_f32_32x32x16_bf16 v[66:81], v[236:239], v[12:15], v[66:81]
	v_add_f32_e32 v164, v177, v164
	v_add_f32_e32 v164, v178, v164
	v_add_f32_e32 v164, v179, v164
	v_add_f32_e32 v164, v180, v164
	v_add_f32_e32 v164, v181, v164
	v_add_f32_e32 v164, v182, v164
	v_add_f32_e32 v164, v183, v164
	s_waitcnt lgkmcnt(3)
	v_mfma_f32_32x32x16_bf16 v[98:113], v[240:243], v[8:11], v[98:113]
	ds_read_b64_tr_b16 v[168:169], v213 offset:40960
	ds_read_b64_tr_b16 v[170:171], v213 offset:41984
	ds_read_b64_tr_b16 v[172:173], v213 offset:43008
	ds_read_b64_tr_b16 v[174:175], v213 offset:44032
	v_add_f32_e32 v164, v82, v164
	v_add_f32_e32 v164, v83, v164
	v_add_f32_e32 v164, v84, v164
	v_add_f32_e32 v164, v85, v164
	s_waitcnt lgkmcnt(6)
	v_mfma_f32_32x32x16_bf16 v[66:81], v[244:247], v[8:11], v[66:81]
	ds_read_b64_tr_b16 v[176:177], v213 offset:45056
	ds_read_b64_tr_b16 v[178:179], v213 offset:46080
	ds_read_b64_tr_b16 v[180:181], v213 offset:47104
	ds_read_b64_tr_b16 v[182:183], v213 offset:48128
	v_add_f32_e32 v164, v86, v164
	v_add_f32_e32 v164, v87, v164
	v_add_f32_e32 v164, v88, v164
	v_add_f32_e32 v164, v89, v164
	s_waitcnt lgkmcnt(9)
	v_mfma_f32_32x32x16_bf16 v[98:113], v[248:251], v[4:7], v[98:113]
	v_add_f32_e32 v164, v90, v164
	v_add_f32_e32 v164, v91, v164
	v_add_f32_e32 v164, v92, v164
	v_add_f32_e32 v164, v93, v164
	s_waitcnt lgkmcnt(8)
	v_mfma_f32_32x32x16_bf16 v[66:81], v[224:227], v[4:7], v[66:81]
	ds_read_b64_tr_b16 v[224:225], v213 offset:41472
	ds_read_b64_tr_b16 v[226:227], v213 offset:42496
	ds_read_b64_tr_b16 v[228:229], v213 offset:43520
	ds_read_b64_tr_b16 v[230:231], v213 offset:44544
	ds_read_b64_tr_b16 v[232:233], v213 offset:45568
	ds_read_b64_tr_b16 v[234:235], v213 offset:46592
	ds_read_b64_tr_b16 v[236:237], v213 offset:47616
	ds_read_b64_tr_b16 v[238:239], v213 offset:48640
	s_waitcnt lgkmcnt(8)
	v_mfma_f32_32x32x16_bf16 v[50:65], v[168:171], v[156:159], v[50:65]
	v_add_f32_e32 v164, v94, v164
	v_add_f32_e32 v164, v95, v164
	v_add_f32_e32 v164, v96, v164
	v_add_f32_e32 v164, v97, v164
	v_mov_b32_e32 v165, v164
	v_mfma_f32_32x32x16_bf16 v[50:65], v[172:175], v[160:163], v[50:65]
	v_cvt_pk_bf16_f32 v82, v82, v83
	v_cvt_pk_bf16_f32 v83, v84, v85
	v_cvt_pk_bf16_f32 v84, v86, v87
	v_cvt_pk_bf16_f32 v85, v88, v89
	v_cvt_pk_bf16_f32 v86, v90, v91
	v_cvt_pk_bf16_f32 v87, v92, v93
	v_cvt_pk_bf16_f32 v88, v94, v95
	v_cvt_pk_bf16_f32 v89, v96, v97
	v_permlane32_swap_b32_e32 v164, v165
	v_mfma_f32_32x32x16_bf16 v[50:65], v[176:179], v[82:85], v[50:65]
	v_mfma_f32_32x32x16_bf16 v[50:65], v[180:183], v[86:89], v[50:65]
	s_cmp_ge_u32 s13, s30
	s_cbranch_scc1 .Lgqa_b_noload_2
	s_cmp_lt_u32 s13, s31
	s_cselect_b32 s9, 0, s31
	s_cselect_b32 s35, s12, s29
	s_lshl_b32 s9, s9, 6
	s_sub_i32 s9, s35, s9
	s_add_i32 s52, s9, s50
	s_add_i32 s52, s52, 64
	s_ashr_i32 s53, s52, 31
	s_lshl_b64 s[52:53], s[52:53], 8
	s_add_u32 s54, s42, s52
	s_addc_u32 s55, s43, s53
	s_add_u32 s56, s44, s52
	s_addc_u32 s57, s45, s53
	global_load_dwordx4 v[118:121], v137, s[54:55]
	global_load_dwordx4 v[122:125], v137, s[56:57]
.Lgqa_b_ld_done_2:
	s_waitcnt lgkmcnt(0)
	v_mfma_f32_32x32x16_bf16 v[34:49], v[224:227], v[156:159], v[34:49]
	s_waitcnt vmcnt(2)
	ds_write_b128 v187, v[130:133] offset:20480
	ds_write_b128 v214, v[126:129] offset:32768
	v_exp_f32_e32 v143, v98
	v_exp_f32_e32 v145, v99
	v_mfma_f32_32x32x16_bf16 v[34:49], v[228:231], v[160:163], v[34:49]
	v_exp_f32_e32 v141, v100
	v_exp_f32_e32 v144, v101
	v_exp_f32_e32 v139, v102
	v_exp_f32_e32 v142, v103
	v_mfma_f32_32x32x16_bf16 v[34:49], v[232:235], v[82:85], v[34:49]
	v_exp_f32_e32 v138, v104
	v_exp_f32_e32 v140, v105
	v_exp_f32_e32 v151, v106
	v_exp_f32_e32 v153, v107
	v_exp_f32_e32 v149, v108
	v_mfma_f32_32x32x16_bf16 v[34:49], v[236:239], v[86:89], v[34:49]
	v_exp_f32_e32 v152, v109
	v_exp_f32_e32 v147, v110
	v_exp_f32_e32 v150, v111
	v_exp_f32_e32 v146, v112
	v_exp_f32_e32 v148, v113
	v_add_f32_e32 v154, v154, v155
	v_add_f32_e32 v136, v136, v154
	v_add_f32_e32 v164, v164, v165
	v_add_f32_e32 v136, v136, v164
	s_add_i32 s13, s13, 2
	s_addk_i32 s50, 0x80
	s_cmp_lt_u32 s8, s0
	s_cbranch_scc1 .LBB0_497
; #define LAS __attribute__((address_space(3)))
; #define SBAR() __builtin_amdgcn_sched_barrier(0)
; __device__ __forceinline__ void finishSM(f32x16& p0, f32x16& p1, float alpha, float& l_reg, bf16x8& pa0, bf16x8& pa1, bf16x8& pa2, bf16x8& pa3) {
; #pragma unroll
;     for (int r = 0; r < 16; ++r) p1[r] = EXP_PROBE ? fmaf(p1[r], 0.001f, 1.f) : __builtin_amdgcn_exp2f(p1[r]);
;     float ps = 0.f;
; #pragma unroll
;     for (int r = 0; r < 16; ++r) ps += p0[r];
; #pragma unroll
;     for (int r = 0; r < 16; ++r) ps += p1[r];
;     { auto rr = __builtin_amdgcn_permlane32_swap(__float_as_uint(ps), __float_as_uint(ps), false, false);
;       ps = __uint_as_float(rr[0]) + __uint_as_float(rr[1]); }
;     l_reg = l_reg * alpha + ps;
;     ATT_PKN(p0, 0, pa0); ATT_PKN(p0, 8, pa1); ATT_PKN(p1, 0, pa2); ATT_PKN(p1, 8, pa3);
; }
; template <int DQK> __device__ __forceinline__ void qkt(f32x16& p0, f32x16& p1, const LAS char* buf, const bf16x8* qr, int r32, int hi, const f32x16& negm) {
; #pragma unroll
;     for (int d0 = 0; d0 < 4; ++d0) { const int ch = d0 * 2 + hi;
;         const bf16x8 b0 = *(const LAS bf16x8*)(buf + B_KN + swz64(r32, ch));
;         const bf16x8 b1 = *(const LAS bf16x8*)(buf + B_KN + swz64(32 + r32, ch));
;         p0 = __builtin_amdgcn_mfma_f32_32x32x16_bf16(b0, qr[d0], d0 == 0 ? negm : p0, 0, 0, 0);
;         p1 = __builtin_amdgcn_mfma_f32_32x32x16_bf16(b1, qr[d0], d0 == 0 ? negm : p1, 0, 0, 0); }
;     if constexpr (DQK == 96) {
; #pragma unroll
;         for (int d0 = 0; d0 < 2; ++d0) { const int ch = d0 * 2 + hi;
;             const bf16x8 b0 = *(const LAS bf16x8*)(buf + B_KR + swz32(r32, ch));
;             const bf16x8 b1 = *(const LAS bf16x8*)(buf + B_KR + swz32(32 + r32, ch));
;             p0 = __builtin_amdgcn_mfma_f32_32x32x16_bf16(b0, qr[4 + d0], p0, 0, 0, 0);
;             p1 = __builtin_amdgcn_mfma_f32_32x32x16_bf16(b1, qr[4 + d0], p1, 0, 0, 0); }
;     }
; template <int DQK, bool FIXM> ...
;     ...
;     __syncthreads();
;     SBAR(); qkt<DQK>(pB0, pB1, lds + bK, qr, r32, hi, negm);
;     finishSM(pA0, pA1, alA, l_reg, pa0, pa1, pa2, pa3); SBAR();
;     if constexpr (FIXM) pv_psm<true>(o0, o1, vb0 + bV, pa0, pa1, pa2, pa3, pB0, pB1, m_reg, negm, alB); else { PVO(bV); partialSM<false>(pB0, pB1, m_reg, negm, alB); }
;     if (!FIXM) RESC(alB);
;     finishSM(pB0, pB1, alB, l_reg, pa0, pa1, pa2, pa3); SBAR();
;     PVO(bK);
.Lgqa_exit_2:
	s_movk_i32 s11, 20480
	s_mov_b32 s10, 0
	s_mov_b32 s1, 40960
	s_mov_b32 s9, s11
	v_add_u32_e32 v2, s11, v213
	s_branch .LBB0_501
.Lgqa_exit_1:
	s_mov_b32 s11, 40960
	s_mov_b32 s10, 20480
	s_mov_b32 s1, 0
	s_mov_b32 s9, s11
	v_add_u32_e32 v2, s11, v213
	s_branch .LBB0_501
.Lgqa_exit_0:
	s_movk_i32 s11, 0
	s_mov_b32 s10, 40960
	s_mov_b32 s1, 20480
	s_mov_b32 s9, s11
	v_add_u32_e32 v2, s11, v213
	s_branch .LBB0_501
.Lgqa_b_noload_0:
	s_waitcnt vmcnt(0)
	s_branch .Lgqa_b_ld_done_0
.Lgqa_b_noload_1:
	s_waitcnt vmcnt(0)
	s_branch .Lgqa_b_ld_done_1
.Lgqa_b_noload_2:
	s_waitcnt vmcnt(0)
	s_branch .Lgqa_b_ld_done_2
.LBB0_501:
	s_lshl_b64 s[0:1], s[4:5], 11
	s_add_u32 s0, s25, s0
	s_addc_u32 s1, s26, s1
	s_lshl_b32 s4, s34, 1
	s_add_u32 s0, s0, s4
	s_addc_u32 s1, s1, 0
	s_waitcnt lgkmcnt(0)
	s_barrier
	v_add_u32_e32 v16, s9, v201
	v_add_u32_e32 v17, v16, v209
	ds_read_b128 v[82:85], v17
	ds_read_b128 v[118:121], v17 offset:4096
	v_add_u32_e32 v86, v16, v210
	v_add_u32_e32 v87, v16, v211
	v_add_u32_e32 v16, v16, v212
	ds_read_b128 v[122:125], v86
	ds_read_b128 v[126:129], v86 offset:4096
	ds_read_b128 v[130:133], v87
	ds_read_b128 v[154:157], v87 offset:4096
	ds_read_b128 v[158:161], v16
	ds_read_b128 v[162:165], v16 offset:4096
	v_exp_f32_e32 v17, v66
	v_exp_f32_e32 v66, v67
	v_exp_f32_e32 v67, v68
	s_waitcnt lgkmcnt(7)
	v_mfma_f32_32x32x16_bf16 v[98:113], v[82:85], v[114:117], v[18:33]
	v_exp_f32_e32 v68, v69
	v_exp_f32_e32 v69, v70
	v_exp_f32_e32 v70, v71
	v_exp_f32_e32 v71, v72
	v_exp_f32_e32 v72, v73
	v_exp_f32_e32 v73, v74
	v_exp_f32_e32 v74, v75
	s_waitcnt lgkmcnt(6)
	v_mfma_f32_32x32x16_bf16 v[82:97], v[118:121], v[114:117], v[18:33]
	v_exp_f32_e32 v75, v76
	v_exp_f32_e32 v76, v77
	v_exp_f32_e32 v77, v78
	v_exp_f32_e32 v78, v79
	v_exp_f32_e32 v79, v80
	v_exp_f32_e32 v80, v81
	s_waitcnt lgkmcnt(5)
	v_mfma_f32_32x32x16_bf16 v[98:113], v[122:125], v[12:15], v[98:113]
	s_waitcnt lgkmcnt(4)
	v_mfma_f32_32x32x16_bf16 v[82:97], v[126:129], v[12:15], v[82:97]
	v_add_f32_e32 v12, 0, v143
	v_add_f32_e32 v12, v145, v12
	v_add_f32_e32 v12, v141, v12
	v_add_f32_e32 v12, v144, v12
	v_add_f32_e32 v12, v139, v12
	v_add_f32_e32 v12, v142, v12
	v_add_f32_e32 v12, v138, v12
	v_add_f32_e32 v12, v140, v12
	v_add_f32_e32 v12, v151, v12
	v_add_f32_e32 v12, v153, v12
	v_add_f32_e32 v12, v149, v12
	v_add_f32_e32 v12, v152, v12
	s_waitcnt lgkmcnt(3)
	v_mfma_f32_32x32x16_bf16 v[98:113], v[130:133], v[8:11], v[98:113]
	s_waitcnt lgkmcnt(2)
	v_mfma_f32_32x32x16_bf16 v[82:97], v[154:157], v[8:11], v[82:97]
	v_add_f32_e32 v8, v147, v12
	v_add_f32_e32 v8, v150, v8
	v_add_f32_e32 v8, v146, v8
	v_add_f32_e32 v8, v148, v8
	v_add_f32_e32 v8, v17, v8
	v_add_f32_e32 v8, v66, v8
	v_add_f32_e32 v8, v67, v8
	v_add_f32_e32 v8, v68, v8
	v_add_f32_e32 v8, v69, v8
	v_add_f32_e32 v8, v70, v8
	v_add_f32_e32 v8, v71, v8
	v_add_f32_e32 v8, v72, v8
	v_add_f32_e32 v8, v73, v8
	v_add_f32_e32 v8, v74, v8
	s_waitcnt lgkmcnt(1)
	v_mfma_f32_32x32x16_bf16 v[98:113], v[158:161], v[4:7], v[98:113]
	s_waitcnt lgkmcnt(0)
	v_mfma_f32_32x32x16_bf16 v[82:97], v[162:165], v[4:7], v[82:97]
	v_add_f32_e32 v4, v75, v8
	v_add_f32_e32 v4, v76, v4
	v_add_f32_e32 v4, v77, v4
	v_add_f32_e32 v4, v78, v4
	v_add_f32_e32 v4, v79, v4
	v_add_f32_e32 v16, v80, v4
	v_mov_b32_e32 v118, v16
	s_nop 1
	v_permlane32_swap_b32_e32 v16, v118
	v_cvt_pk_bf16_f32 v4, v143, v145
	v_cvt_pk_bf16_f32 v5, v141, v144
	v_cvt_pk_bf16_f32 v6, v139, v142
	v_cvt_pk_bf16_f32 v7, v138, v140
	v_cvt_pk_bf16_f32 v8, v151, v153
	v_cvt_pk_bf16_f32 v9, v149, v152
	v_cvt_pk_bf16_f32 v10, v147, v150
	v_cvt_pk_bf16_f32 v11, v146, v148
	v_cvt_pk_bf16_f32 v12, v17, v66
	v_cvt_pk_bf16_f32 v13, v67, v68
	v_cvt_pk_bf16_f32 v14, v69, v70
	v_cvt_pk_bf16_f32 v15, v71, v72
	v_cvt_pk_bf16_f32 v66, v73, v74
	v_cvt_pk_bf16_f32 v67, v75, v76
	v_cvt_pk_bf16_f32 v68, v77, v78
	v_cvt_pk_bf16_f32 v69, v79, v80
	v_add_u32_e32 v17, s10, v213
	ds_read_b64_tr_b16 v[70:71], v17 offset:0
	ds_read_b64_tr_b16 v[72:73], v17 offset:0x400
	ds_read_b64_tr_b16 v[74:75], v17 offset:0x800
	ds_read_b64_tr_b16 v[76:77], v17 offset:0xc00
	ds_read_b64_tr_b16 v[78:79], v17 offset:0x1000
	ds_read_b64_tr_b16 v[80:81], v17 offset:0x1400
	ds_read_b64_tr_b16 v[114:115], v17 offset:0x1800
	ds_read_b64_tr_b16 v[116:117], v17 offset:0x1c00
	v_exp_f32_e32 v120, v98
	v_exp_f32_e32 v121, v99
	v_exp_f32_e32 v122, v100
	v_exp_f32_e32 v123, v101
	v_exp_f32_e32 v102, v102
	v_exp_f32_e32 v103, v103
	v_exp_f32_e32 v104, v104
	v_exp_f32_e32 v105, v105
	s_waitcnt lgkmcnt(0)
	v_mfma_f32_32x32x16_bf16 v[50:65], v[70:73], v[4:7], v[50:65]
	v_mfma_f32_32x32x16_bf16 v[50:65], v[74:77], v[8:11], v[50:65]
	v_mfma_f32_32x32x16_bf16 v[50:65], v[78:81], v[12:15], v[50:65]
	v_mfma_f32_32x32x16_bf16 v[50:65], v[114:117], v[66:69], v[50:65]
	ds_read_b64_tr_b16 v[70:71], v17 offset:0x200
	ds_read_b64_tr_b16 v[72:73], v17 offset:0x600
	ds_read_b64_tr_b16 v[74:75], v17 offset:0xa00
	ds_read_b64_tr_b16 v[76:77], v17 offset:0xe00
	ds_read_b64_tr_b16 v[78:79], v17 offset:0x1200
	ds_read_b64_tr_b16 v[80:81], v17 offset:0x1600
	ds_read_b64_tr_b16 v[98:99], v17 offset:0x1a00
	ds_read_b64_tr_b16 v[100:101], v17 offset:0x1e00
	v_exp_f32_e32 v106, v106
	v_exp_f32_e32 v107, v107
	v_exp_f32_e32 v108, v108
	v_exp_f32_e32 v109, v109
	v_exp_f32_e32 v110, v110
	v_exp_f32_e32 v111, v111
	v_exp_f32_e32 v112, v112
	v_exp_f32_e32 v113, v113
	s_waitcnt lgkmcnt(0)
; #define SBAR() __builtin_amdgcn_sched_barrier(0)
; __device__ __forceinline__ unsigned cvt_pk_bf16(float lo, float hi) { unsigned r; asm volatile("v_cvt_pk_bf16_f32 %0, %1, %2" : "=v"(r) : "v"(lo), "v"(hi)); return r; }
; #define PVO(boff) do { pv_one<0>(o0, vb0 + (boff), pa0, pa1, pa2, pa3); pv_one<1>(o1, vb0 + (boff), pa0, pa1, pa2, pa3); } while (0)
; #define RESC(a) do { if (__any((a) < 1.f)) { _Pragma("unroll") for (int r = 0; r < 16; ++r) { o0[r] *= (a); o1[r] *= (a); } } } while (0)
; template <int DQK, bool FIXM> ...
;     ...
;     if constexpr (FIXM) pv_psm<true>(o0, o1, vb0 + bV, pa0, pa1, pa2, pa3, pB0, pB1, m_reg, negm, alB); else { PVO(bV); partialSM<false>(pB0, pB1, m_reg, negm, alB); }
;     if (!FIXM) RESC(alB);
;     finishSM(pB0, pB1, alB, l_reg, pa0, pa1, pa2, pa3); SBAR();
;     PVO(bK);
;     ...
;     const float inv = __builtin_amdgcn_rcpf(l_reg);
;     bf16_t* Ow = Op + (size_t)(wid * 32 + r32) * 1024 + 4 * hi;
; #pragma unroll
;     for (int g = 0; g < 4; ++g) {
;         u32x2 w0, w1;
;         w0.x = cvt_pk_bf16(o0[4 * g] * inv, o0[4 * g + 1] * inv); w0.y = cvt_pk_bf16(o0[4 * g + 2] * inv, o0[4 * g + 3] * inv);
;         w1.x = cvt_pk_bf16(o1[4 * g] * inv, o1[4 * g + 1] * inv); w1.y = cvt_pk_bf16(o1[4 * g + 2] * inv, o1[4 * g + 3] * inv);
;         *(u32x2*)(Ow + 8 * g) = w0; *(u32x2*)(Ow + 32 + 8 * g) = w1;
;     }
	v_mfma_f32_32x32x16_bf16 v[34:49], v[70:73], v[4:7], v[34:49]
	v_add_f32_e32 v4, 0, v120
	v_add_f32_e32 v4, v121, v4
	v_add_f32_e32 v4, v122, v4
	v_add_f32_e32 v4, v123, v4
	v_add_f32_e32 v4, v102, v4
	v_add_f32_e32 v4, v103, v4
	v_add_f32_e32 v4, v104, v4
	v_add_f32_e32 v4, v105, v4
	v_add_f32_e32 v4, v106, v4
	v_add_f32_e32 v4, v107, v4
	v_add_f32_e32 v4, v108, v4
	v_add_f32_e32 v4, v109, v4
	v_exp_f32_e32 v82, v82
	v_add_f32_e32 v4, v110, v4
	v_exp_f32_e32 v83, v83
	v_add_f32_e32 v4, v111, v4
	v_exp_f32_e32 v84, v84
	v_add_f32_e32 v4, v112, v4
	v_exp_f32_e32 v85, v85
	v_add_f32_e32 v4, v113, v4
	v_exp_f32_e32 v86, v86
	v_add_f32_e32 v4, v82, v4
	v_exp_f32_e32 v87, v87
	v_add_f32_e32 v4, v83, v4
	v_exp_f32_e32 v70, v88
	v_add_f32_e32 v4, v84, v4
	v_exp_f32_e32 v71, v89
	v_add_f32_e32 v4, v85, v4
	v_exp_f32_e32 v72, v90
	v_mfma_f32_32x32x16_bf16 v[34:49], v[74:77], v[8:11], v[34:49]
	v_add_f32_e32 v4, v86, v4
	v_exp_f32_e32 v73, v91
	v_add_f32_e32 v4, v87, v4
	v_exp_f32_e32 v88, v92
	v_add_f32_e32 v4, v70, v4
	v_exp_f32_e32 v89, v93
	v_add_f32_e32 v4, v71, v4
	v_exp_f32_e32 v90, v94
	v_add_f32_e32 v4, v72, v4
	v_exp_f32_e32 v74, v95
	v_add_f32_e32 v4, v73, v4
	v_exp_f32_e32 v75, v96
	v_add_f32_e32 v4, v88, v4
	v_exp_f32_e32 v76, v97
	v_add_f32_e32 v4, v89, v4
	v_mfma_f32_32x32x16_bf16 v[34:49], v[78:81], v[12:15], v[34:49]
	v_add_f32_e32 v4, v90, v4
	v_add_f32_e32 v4, v74, v4
	v_add_f32_e32 v4, v75, v4
	v_add_f32_e32 v17, v76, v4
	v_mov_b32_e32 v119, v17
	s_nop 1
	v_permlane32_swap_b32_e32 v17, v119
	v_pk_add_f32 v[4:5], v[16:17], v[118:119]
	v_mfma_f32_32x32x16_bf16 v[34:49], v[98:101], v[66:69], v[34:49]
	v_add_f32_e32 v4, v136, v4
	v_add_f32_e32 v16, v4, v5
	v_cvt_pk_bf16_f32 v4, v120, v121
	v_cvt_pk_bf16_f32 v5, v122, v123
	v_cvt_pk_bf16_f32 v6, v102, v103
	v_cvt_pk_bf16_f32 v7, v104, v105
	v_cvt_pk_bf16_f32 v8, v106, v107
	v_cvt_pk_bf16_f32 v9, v108, v109
	v_cvt_pk_bf16_f32 v10, v110, v111
	v_cvt_pk_bf16_f32 v11, v112, v113
	v_cvt_pk_bf16_f32 v12, v82, v83
	v_cvt_pk_bf16_f32 v13, v84, v85
	v_cvt_pk_bf16_f32 v14, v86, v87
	v_cvt_pk_bf16_f32 v15, v70, v71
	v_cvt_pk_bf16_f32 v66, v72, v73
	v_cvt_pk_bf16_f32 v67, v88, v89
	v_cvt_pk_bf16_f32 v68, v90, v74
	v_cvt_pk_bf16_f32 v69, v75, v76
	ds_read_b64_tr_b16 v[70:71], v2 offset:0
	ds_read_b64_tr_b16 v[72:73], v2 offset:0x400
	ds_read_b64_tr_b16 v[74:75], v2 offset:0x800
	ds_read_b64_tr_b16 v[76:77], v2 offset:0xc00
	ds_read_b64_tr_b16 v[78:79], v2 offset:0x1000
	ds_read_b64_tr_b16 v[80:81], v2 offset:0x1400
	ds_read_b64_tr_b16 v[82:83], v2 offset:0x1800
	ds_read_b64_tr_b16 v[84:85], v2 offset:0x1c00
	s_waitcnt lgkmcnt(0)
	s_nop 0
	v_mfma_f32_32x32x16_bf16 v[50:65], v[70:73], v[4:7], v[50:65]
	ds_read_b64_tr_b16 v[70:71], v2 offset:0x200
	ds_read_b64_tr_b16 v[72:73], v2 offset:0x600
	v_mfma_f32_32x32x16_bf16 v[50:65], v[74:77], v[8:11], v[50:65]
	ds_read_b64_tr_b16 v[74:75], v2 offset:0xa00
	ds_read_b64_tr_b16 v[76:77], v2 offset:0xe00
	v_mfma_f32_32x32x16_bf16 v[50:65], v[78:81], v[12:15], v[50:65]
	ds_read_b64_tr_b16 v[78:79], v2 offset:0x1200
	ds_read_b64_tr_b16 v[80:81], v2 offset:0x1600
	ds_read_b64_tr_b16 v[86:87], v2 offset:0x1a00
	ds_read_b64_tr_b16 v[88:89], v2 offset:0x1e00
	s_waitcnt lgkmcnt(0)
	v_mfma_f32_32x32x16_bf16 v[50:65], v[82:85], v[66:69], v[50:65]
	v_mfma_f32_32x32x16_bf16 v[34:49], v[70:73], v[4:7], v[34:49]
	v_rcp_f32_e32 v16, v16
	v_lshl_add_u64 v[4:5], s[0:1], 0, v[194:195]
	v_lshlrev_b32_e32 v2, 1, v190
	v_lshl_add_u64 v[6:7], v[4:5], 0, v[2:3]
	s_nop 6
	v_mul_f32_e32 v2, v16, v50
	v_lshl_add_u64 v[4:5], v[6:7], 0, s[6:7]
	s_mov_b64 s[0:1], 0
	v_mfma_f32_32x32x16_bf16 v[34:49], v[74:77], v[8:11], v[34:49]
	v_mul_f32_e32 v8, v16, v51
	v_mul_f32_e32 v9, v16, v53
	v_cvt_pk_bf16_f32 v8, v2, v8
	v_mul_f32_e32 v2, v16, v52
	v_cvt_pk_bf16_f32 v9, v2, v9
	v_mfma_f32_32x32x16_bf16 v[34:49], v[78:81], v[12:15], v[34:49]
	v_mul_f32_e32 v12, v16, v54
	v_mul_f32_e32 v13, v16, v55
	v_mul_f32_e32 v14, v16, v56
	v_mul_f32_e32 v15, v16, v57
	v_mfma_f32_32x32x16_bf16 v[34:49], v[86:89], v[66:69], v[34:49]
	s_nop 11
	v_mul_f32_e32 v10, v16, v35
	v_mul_f32_e32 v11, v16, v36
	v_mul_f32_e32 v2, v16, v34
	v_mul_f32_e32 v17, v16, v37
	v_cvt_pk_bf16_f32 v10, v2, v10
	v_cvt_pk_bf16_f32 v11, v11, v17
	global_store_dwordx2 v[6:7], v[8:9], off offset:1024
	global_store_dwordx2 v[6:7], v[10:11], off offset:1088
	v_cvt_pk_bf16_f32 v8, v12, v13
	v_cvt_pk_bf16_f32 v9, v14, v15
	v_mul_f32_e32 v34, v16, v38
	v_mul_f32_e32 v35, v16, v39
	v_mul_f32_e32 v36, v16, v40
	v_mul_f32_e32 v37, v16, v41
	v_cvt_pk_bf16_f32 v10, v34, v35
	v_cvt_pk_bf16_f32 v11, v36, v37
	global_store_dwordx2 v[6:7], v[8:9], off offset:1040
	global_store_dwordx2 v[6:7], v[10:11], off offset:1104
	v_mul_f32_e32 v2, v16, v58
	v_mul_f32_e32 v8, v16, v59
	v_cvt_pk_bf16_f32 v8, v2, v8
	v_mul_f32_e32 v2, v16, v60
	v_mul_f32_e32 v9, v16, v61
	v_cvt_pk_bf16_f32 v9, v2, v9
	v_mul_f32_e32 v2, v16, v42
	v_mul_f32_e32 v10, v16, v43
	v_cvt_pk_bf16_f32 v10, v2, v10
	v_mul_f32_e32 v2, v16, v44
	v_mul_f32_e32 v11, v16, v45
	v_cvt_pk_bf16_f32 v11, v2, v11
	global_store_dwordx2 v[6:7], v[8:9], off offset:1056
	global_store_dwordx2 v[6:7], v[10:11], off offset:1120
	v_mul_f32_e32 v2, v16, v62
	v_mul_f32_e32 v6, v16, v63
	v_cvt_pk_bf16_f32 v6, v2, v6
	v_mul_f32_e32 v2, v16, v64
	v_mul_f32_e32 v7, v16, v65
	v_cvt_pk_bf16_f32 v7, v2, v7
	v_mul_f32_e32 v2, v16, v46
	v_mul_f32_e32 v8, v16, v47
	v_mul_f32_e32 v9, v16, v49
	v_cvt_pk_bf16_f32 v8, v2, v8
	v_mul_f32_e32 v2, v16, v48
	v_cvt_pk_bf16_f32 v9, v2, v9
